# v70 + the five bf16 GEMM loops with a zeroing block peeled the same way (first MFMA into each accumulator block takes C=0)
# baseline (speedup 1.0000x reference)
; #define PG8_STAGE(bufoff, gbase, voff) do { _Pragma("unroll") for (int _i = 0; _i < 2; ++_i) \
;         __builtin_amdgcn_global_load_lds((const unsigned*)((const char*)(gbase) + (voff)[_i]), (PG8_LAS unsigned*)(lds + (bufoff) + ldsw + _i * 8192), 16, 0, 0); } while (0)
; #define PG8_WAIT_V(n) asm volatile("s_waitcnt vmcnt(" #n ")" ::: "memory")
; #define PG8_WAIT_L(n) asm volatile("s_waitcnt lgkmcnt(" #n ")" ::: "memory")
; #define PG8_BAR __builtin_amdgcn_s_barrier()
; #define PG8_SCHED __builtin_amdgcn_sched_barrier(0)
; template <class Epi, class Sched, bool ALIGN_EPI = true, bool F8 = false>
; __device__ __forceinline__ void gemm_phase(PG8_LAS unsigned char* lds, const Sched& S, const Epi& E) {
;     ...
;             PG8_LDB(B0, 0, 0); PG8_LDB(B1, 0, 1); PG8_SCHED; PG8_LDA(At, 0, 0); PG8_STAGE(PG8_SA(1, 1), a1, voffA[1]);
;             PG8_WAIT_V(8); PG8_WAIT_L(0); PG8_BAR; PG8_MMA(0, 0, At, B0); PG8_MMA(0, 1, At, B1); PG8_BAR; PG8_SCHED;
;             PG8_LDA(At, 0, 1); PG8_STAGE(PG8_SB(0, 0), b2, voffB[0]); PG8_STAGE(PG8_SB(0, 1), b2, voffB[1]); PG8_STAGE(PG8_SA(0, 0), a2, vA2[0]);
;             PG8_WAIT_V(8); PG8_WAIT_L(0); PG8_BAR; PG8_MMA(1, 0, At, B0); PG8_MMA(1, 1, At, B1); PG8_BAR; PG8_SCHED;
;     ...
;         for (int a = 0; a < 2; ++a)
; #pragma unroll
;             for (int b = 0; b < 2; ++b)
; #pragma unroll
;                 for (int m = 0; m < 4; ++m)
; #pragma unroll
;                     for (int n = 0; n < 2; ++n) acc[a][b][m][n] = (f32x4){0.f, 0.f, 0.f, 0.f};
.LBB0_490:
	s_add_u32 s15, s24, 0x100
	s_addc_u32 s65, s25, 0
	s_mov_b32 s66, -2
.Lpkb_491:
	ds_read_b128 v[178:181], v173
	ds_read_b128 v[182:185], v173 offset:1024
	ds_read_b128 v[186:189], v173 offset:2048
	ds_read_b128 v[190:193], v173 offset:3072
	ds_read_b128 v[194:197], v174
	ds_read_b128 v[198:201], v174 offset:1024
	ds_read_b128 v[202:205], v174 offset:2048
	ds_read_b128 v[206:209], v174 offset:3072
	s_add_u32 s24, s22, 0x100
	s_addc_u32 s25, s23, 0
	s_cmp_eq_u32 s66, 4
	s_cselect_b32 s29, s17, s25
	s_cselect_b32 s28, s16, s24
	s_cselect_b32 s27, s19, s65
	s_cselect_b32 s26, s18, s15
	s_mov_b32 m0, s49
	v_lshl_add_u64 v[242:243], s[22:23], 0, v[166:167]
	ds_read_b128 v[210:213], v175
	ds_read_b128 v[214:217], v175 offset:1024
	ds_read_b128 v[218:221], v175 offset:2048
	ds_read_b128 v[222:225], v175 offset:3072
	ds_read_b128 v[226:229], v175 offset:4096
	ds_read_b128 v[230:233], v175 offset:5120
	ds_read_b128 v[234:237], v175 offset:6144
	ds_read_b128 v[238:241], v175 offset:7168
	global_load_lds_dwordx4 v[242:243], off
	v_lshl_add_u64 v[242:243], s[22:23], 0, v[164:165]
	s_mov_b32 m0, s50
	s_nop 0
	global_load_lds_dwordx4 v[242:243], off
	s_waitcnt vmcnt(8)
	s_waitcnt lgkmcnt(0)
	s_barrier
	s_setprio 1
	s_waitcnt lgkmcnt(0)
	v_mfma_f32_16x16x32_bf16 v[126:129], v[178:181], v[210:213], 0
	v_mfma_f32_16x16x32_bf16 v[122:125], v[186:189], v[210:213], 0
	v_mfma_f32_16x16x32_bf16 v[118:121], v[178:181], v[218:221], 0
	v_mfma_f32_16x16x32_bf16 v[114:117], v[186:189], v[218:221], 0
	v_mfma_f32_16x16x32_bf16 v[110:113], v[178:181], v[226:229], 0
	v_mfma_f32_16x16x32_bf16 v[106:109], v[186:189], v[226:229], 0
	v_mfma_f32_16x16x32_bf16 v[98:101], v[178:181], v[234:237], 0
	v_mfma_f32_16x16x32_bf16 v[90:93], v[186:189], v[234:237], 0
	v_mfma_f32_16x16x32_bf16 v[126:129], v[182:185], v[214:217], v[126:129]
	v_mfma_f32_16x16x32_bf16 v[122:125], v[190:193], v[214:217], v[122:125]
	v_mfma_f32_16x16x32_bf16 v[118:121], v[182:185], v[222:225], v[118:121]
	v_mfma_f32_16x16x32_bf16 v[114:117], v[190:193], v[222:225], v[114:117]
	v_mfma_f32_16x16x32_bf16 v[110:113], v[182:185], v[230:233], v[110:113]
	v_mfma_f32_16x16x32_bf16 v[106:109], v[190:193], v[230:233], v[106:109]
	v_mfma_f32_16x16x32_bf16 v[98:101], v[182:185], v[238:241], v[98:101]
	v_mfma_f32_16x16x32_bf16 v[90:93], v[190:193], v[238:241], v[90:93]
	s_setprio 0
	s_setprio 1
	v_mfma_f32_16x16x32_bf16 v[102:105], v[194:197], v[210:213], 0
	v_mfma_f32_16x16x32_bf16 v[94:97], v[202:205], v[210:213], 0
	v_mfma_f32_16x16x32_bf16 v[86:89], v[194:197], v[218:221], 0
	v_mfma_f32_16x16x32_bf16 v[82:85], v[202:205], v[218:221], 0
	v_mfma_f32_16x16x32_bf16 v[78:81], v[194:197], v[226:229], 0
	v_mfma_f32_16x16x32_bf16 v[74:77], v[202:205], v[226:229], 0
	v_mfma_f32_16x16x32_bf16 v[70:73], v[194:197], v[234:237], 0
	v_mfma_f32_16x16x32_bf16 v[66:69], v[202:205], v[234:237], 0
	v_mfma_f32_16x16x32_bf16 v[102:105], v[198:201], v[214:217], v[102:105]
	v_mfma_f32_16x16x32_bf16 v[94:97], v[206:209], v[214:217], v[94:97]
	v_mfma_f32_16x16x32_bf16 v[86:89], v[198:201], v[222:225], v[86:89]
	v_mfma_f32_16x16x32_bf16 v[82:85], v[206:209], v[222:225], v[82:85]
	v_mfma_f32_16x16x32_bf16 v[78:81], v[198:201], v[230:233], v[78:81]
	v_mfma_f32_16x16x32_bf16 v[74:77], v[206:209], v[230:233], v[74:77]
	v_mfma_f32_16x16x32_bf16 v[70:73], v[198:201], v[238:241], v[70:73]
	v_mfma_f32_16x16x32_bf16 v[66:69], v[206:209], v[238:241], v[66:69]
	s_setprio 0
	s_barrier
	s_mov_b32 m0, s51
	v_lshl_add_u64 v[242:243], s[26:27], 0, v[134:135]
	ds_read_b128 v[210:213], v175 offset:16384
	ds_read_b128 v[214:217], v175 offset:17408
	ds_read_b128 v[218:221], v175 offset:18432
	ds_read_b128 v[222:225], v175 offset:19456
	ds_read_b128 v[226:229], v175 offset:20480
	ds_read_b128 v[230:233], v175 offset:21504
	ds_read_b128 v[234:237], v175 offset:22528
	ds_read_b128 v[238:241], v175 offset:23552
	global_load_lds_dwordx4 v[242:243], off
	v_lshl_add_u64 v[244:245], s[26:27], 0, v[130:131]
	s_mov_b32 m0, s52
	v_lshl_add_u64 v[246:247], s[26:27], 0, v[136:137]
	global_load_lds_dwordx4 v[244:245], off
	s_mov_b32 m0, s53
	v_lshl_add_u64 v[248:249], s[28:29], 0, v[140:141]
	global_load_lds_dwordx4 v[246:247], off
	v_lshl_add_u64 v[246:247], s[26:27], 0, v[132:133]
	s_mov_b32 m0, s59
	s_nop 0
	global_load_lds_dwordx4 v[246:247], off
	v_lshl_add_u64 v[246:247], s[28:29], 0, v[138:139]
	s_mov_b32 m0, s42
	s_nop 0
	global_load_lds_dwordx4 v[246:247], off
	s_mov_b32 m0, s43
	s_nop 0
	global_load_lds_dwordx4 v[248:249], off
	s_waitcnt vmcnt(8)
	s_waitcnt lgkmcnt(0)
	s_barrier
	s_setprio 1
	s_waitcnt lgkmcnt(0)
	v_mfma_f32_16x16x32_bf16 v[62:65], v[178:181], v[210:213], 0
	v_mfma_f32_16x16x32_bf16 v[58:61], v[186:189], v[210:213], 0
	v_mfma_f32_16x16x32_bf16 v[54:57], v[178:181], v[218:221], 0
	v_mfma_f32_16x16x32_bf16 v[50:53], v[186:189], v[218:221], 0
	v_mfma_f32_16x16x32_bf16 v[46:49], v[178:181], v[226:229], 0
	v_mfma_f32_16x16x32_bf16 v[42:45], v[186:189], v[226:229], 0
	v_mfma_f32_16x16x32_bf16 v[34:37], v[178:181], v[234:237], 0
	v_mfma_f32_16x16x32_bf16 v[26:29], v[186:189], v[234:237], 0
	v_mfma_f32_16x16x32_bf16 v[62:65], v[182:185], v[214:217], v[62:65]
	v_mfma_f32_16x16x32_bf16 v[58:61], v[190:193], v[214:217], v[58:61]
	v_mfma_f32_16x16x32_bf16 v[54:57], v[182:185], v[222:225], v[54:57]
	v_mfma_f32_16x16x32_bf16 v[50:53], v[190:193], v[222:225], v[50:53]
	v_mfma_f32_16x16x32_bf16 v[46:49], v[182:185], v[230:233], v[46:49]
	v_mfma_f32_16x16x32_bf16 v[42:45], v[190:193], v[230:233], v[42:45]
	v_mfma_f32_16x16x32_bf16 v[34:37], v[182:185], v[238:241], v[34:37]
	v_mfma_f32_16x16x32_bf16 v[26:29], v[190:193], v[238:241], v[26:29]
	s_setprio 0
	s_setprio 1
	v_mfma_f32_16x16x32_bf16 v[38:41], v[194:197], v[210:213], 0
	v_mfma_f32_16x16x32_bf16 v[30:33], v[202:205], v[210:213], 0
	v_mfma_f32_16x16x32_bf16 v[22:25], v[194:197], v[218:221], 0
	v_mfma_f32_16x16x32_bf16 v[18:21], v[202:205], v[218:221], 0
	v_mfma_f32_16x16x32_bf16 v[14:17], v[194:197], v[226:229], 0
	v_mfma_f32_16x16x32_bf16 v[10:13], v[202:205], v[226:229], 0
	v_mfma_f32_16x16x32_bf16 v[6:9], v[194:197], v[234:237], 0
	v_mfma_f32_16x16x32_bf16 v[2:5], v[202:205], v[234:237], 0
	v_mfma_f32_16x16x32_bf16 v[38:41], v[198:201], v[214:217], v[38:41]
	v_mfma_f32_16x16x32_bf16 v[30:33], v[206:209], v[214:217], v[30:33]
	v_mfma_f32_16x16x32_bf16 v[22:25], v[198:201], v[222:225], v[22:25]
	v_mfma_f32_16x16x32_bf16 v[18:21], v[206:209], v[222:225], v[18:21]
	v_mfma_f32_16x16x32_bf16 v[14:17], v[198:201], v[230:233], v[14:17]
	v_mfma_f32_16x16x32_bf16 v[10:13], v[206:209], v[230:233], v[10:13]
	v_mfma_f32_16x16x32_bf16 v[6:9], v[198:201], v[238:241], v[6:9]
	v_mfma_f32_16x16x32_bf16 v[2:5], v[206:209], v[238:241], v[2:5]
	s_setprio 0
	s_barrier
; #define PG8_STAGE(bufoff, gbase, voff) do { _Pragma("unroll") for (int _i = 0; _i < 2; ++_i) \
;         __builtin_amdgcn_global_load_lds((const unsigned*)((const char*)(gbase) + (voff)[_i]), (PG8_LAS unsigned*)(lds + (bufoff) + ldsw + _i * 8192), 16, 0, 0); } while (0)
; #define PG8_WAIT_V(n) asm volatile("s_waitcnt vmcnt(" #n ")" ::: "memory")
; #define PG8_WAIT_L(n) asm volatile("s_waitcnt lgkmcnt(" #n ")" ::: "memory")
; template <class Epi, class Sched, bool ALIGN_EPI = true, bool F8 = false>
; __device__ __forceinline__ void gemm_phase(PG8_LAS unsigned char* lds, const Sched& S, const Epi& E) {
;     ...
;         for (int t = 0; t < nt; t += 2) {
;             const bool last = (t == nt - 2);
;             if constexpr (Sched::GATHER) { if (last && has_next) S.a_off(nxt, Rs, Cs, voffAn); }
;             const char* a1 = cA + (size_t)(t + 1) * kstep;
;             const char* a2 = last ? nA : cA + (size_t)(t + 2) * kstep; const char* b2 = last ? nB : cB + (size_t)(t + 2) * kstepB;
;             const char* a3 = a2 + kstep; const char* b3 = b2 + kstepB;
;             unsigned vA2[2][2];
; #pragma unroll
;             for (int h = 0; h < 2; ++h)
; #pragma unroll
;                 for (int i = 0; i < 2; ++i) { if constexpr (Sched::GATHER) vA2[h][i] = (last && has_next) ? voffAn[h][i] : voffA[h][i]; else vA2[h][i] = voffA[h][i]; }
;             PG8_LDB(B0, 0, 0); PG8_LDB(B1, 0, 1); PG8_SCHED; PG8_LDA(At, 0, 0); PG8_STAGE(PG8_SA(1, 1), a1, voffA[1]);
;             PG8_WAIT_V(8); PG8_WAIT_L(0); PG8_BAR; PG8_MMA(0, 0, At, B0); PG8_MMA(0, 1, At, B1); PG8_BAR; PG8_SCHED;
;             PG8_LDA(At, 0, 1); PG8_STAGE(PG8_SB(0, 0), b2, voffB[0]); PG8_STAGE(PG8_SB(0, 1), b2, voffB[1]); PG8_STAGE(PG8_SA(0, 0), a2, vA2[0]);
;             PG8_WAIT_V(8); PG8_WAIT_L(0); PG8_BAR; PG8_MMA(1, 0, At, B0); PG8_MMA(1, 1, At, B1); PG8_BAR; PG8_SCHED;
;             PG8_LDB(B0, 1, 0); PG8_LDB(B1, 1, 1); PG8_SCHED; PG8_LDA(At, 1, 0); PG8_STAGE(PG8_SA(0, 1), a2, vA2[1]);
;             PG8_WAIT_V(8); PG8_WAIT_L(0); PG8_BAR; PG8_MMA(0, 0, At, B0); PG8_MMA(0, 1, At, B1); PG8_BAR; PG8_SCHED;
;             PG8_LDA(At, 1, 1); PG8_STAGE(PG8_SB(1, 0), b3, voffB[0]); PG8_STAGE(PG8_SB(1, 1), b3, voffB[1]); PG8_STAGE(PG8_SA(1, 0), a3, vA2[0]);
;             PG8_WAIT_V(8); PG8_WAIT_L(0); PG8_BAR; PG8_MMA(1, 0, At, B0); PG8_MMA(1, 1, At, B1); PG8_BAR; PG8_SCHED;
	ds_read_b128 v[178:181], v176
	ds_read_b128 v[182:185], v176 offset:1024
	ds_read_b128 v[186:189], v176 offset:2048
	ds_read_b128 v[190:193], v176 offset:3072
	ds_read_b128 v[194:197], v177
	ds_read_b128 v[198:201], v177 offset:1024
	ds_read_b128 v[202:205], v177 offset:2048
	ds_read_b128 v[206:209], v177 offset:3072
	s_mov_b32 m0, s44
	v_lshl_add_u64 v[250:251], s[28:29], 0, v[142:143]
	ds_read_b128 v[210:213], v175 offset:32768
	ds_read_b128 v[214:217], v175 offset:33792
	ds_read_b128 v[218:221], v175 offset:34816
	ds_read_b128 v[222:225], v175 offset:35840
	ds_read_b128 v[226:229], v175 offset:36864
	ds_read_b128 v[230:233], v175 offset:37888
	ds_read_b128 v[234:237], v175 offset:38912
	ds_read_b128 v[238:241], v175 offset:39936
	global_load_lds_dwordx4 v[250:251], off
	v_lshl_add_u64 v[250:251], s[28:29], 0, v[144:145]
	s_mov_b32 m0, s45
	s_nop 0
	global_load_lds_dwordx4 v[250:251], off
	s_waitcnt vmcnt(8)
	s_waitcnt lgkmcnt(0)
	s_barrier
	s_setprio 1
	s_waitcnt lgkmcnt(0)
	v_mfma_f32_16x16x32_bf16 v[126:129], v[178:181], v[210:213], v[126:129]
	v_mfma_f32_16x16x32_bf16 v[122:125], v[186:189], v[210:213], v[122:125]
	v_mfma_f32_16x16x32_bf16 v[118:121], v[178:181], v[218:221], v[118:121]
	v_mfma_f32_16x16x32_bf16 v[114:117], v[186:189], v[218:221], v[114:117]
	v_mfma_f32_16x16x32_bf16 v[110:113], v[178:181], v[226:229], v[110:113]
	v_mfma_f32_16x16x32_bf16 v[106:109], v[186:189], v[226:229], v[106:109]
	v_mfma_f32_16x16x32_bf16 v[98:101], v[178:181], v[234:237], v[98:101]
	v_mfma_f32_16x16x32_bf16 v[90:93], v[186:189], v[234:237], v[90:93]
	v_mfma_f32_16x16x32_bf16 v[126:129], v[182:185], v[214:217], v[126:129]
	v_mfma_f32_16x16x32_bf16 v[122:125], v[190:193], v[214:217], v[122:125]
	v_mfma_f32_16x16x32_bf16 v[118:121], v[182:185], v[222:225], v[118:121]
	v_mfma_f32_16x16x32_bf16 v[114:117], v[190:193], v[222:225], v[114:117]
	v_mfma_f32_16x16x32_bf16 v[110:113], v[182:185], v[230:233], v[110:113]
	v_mfma_f32_16x16x32_bf16 v[106:109], v[190:193], v[230:233], v[106:109]
	v_mfma_f32_16x16x32_bf16 v[98:101], v[182:185], v[238:241], v[98:101]
	v_mfma_f32_16x16x32_bf16 v[90:93], v[190:193], v[238:241], v[90:93]
	s_setprio 0
	s_setprio 1
	v_mfma_f32_16x16x32_bf16 v[102:105], v[194:197], v[210:213], v[102:105]
	v_mfma_f32_16x16x32_bf16 v[94:97], v[202:205], v[210:213], v[94:97]
	v_mfma_f32_16x16x32_bf16 v[86:89], v[194:197], v[218:221], v[86:89]
	v_mfma_f32_16x16x32_bf16 v[82:85], v[202:205], v[218:221], v[82:85]
	v_mfma_f32_16x16x32_bf16 v[78:81], v[194:197], v[226:229], v[78:81]
	v_mfma_f32_16x16x32_bf16 v[74:77], v[202:205], v[226:229], v[74:77]
	v_mfma_f32_16x16x32_bf16 v[70:73], v[194:197], v[234:237], v[70:73]
	v_mfma_f32_16x16x32_bf16 v[66:69], v[202:205], v[234:237], v[66:69]
	v_mfma_f32_16x16x32_bf16 v[102:105], v[198:201], v[214:217], v[102:105]
	v_mfma_f32_16x16x32_bf16 v[94:97], v[206:209], v[214:217], v[94:97]
	v_mfma_f32_16x16x32_bf16 v[86:89], v[198:201], v[222:225], v[86:89]
	v_mfma_f32_16x16x32_bf16 v[82:85], v[206:209], v[222:225], v[82:85]
	v_mfma_f32_16x16x32_bf16 v[78:81], v[198:201], v[230:233], v[78:81]
	v_mfma_f32_16x16x32_bf16 v[74:77], v[206:209], v[230:233], v[74:77]
	v_mfma_f32_16x16x32_bf16 v[70:73], v[198:201], v[238:241], v[70:73]
	v_mfma_f32_16x16x32_bf16 v[66:69], v[206:209], v[238:241], v[66:69]
	s_setprio 0
	s_barrier
	s_mov_b32 m0, s60
	s_add_u32 s22, s26, 0x80
	v_lshl_add_u64 v[242:243], v[242:243], 0, s[8:9]
	ds_read_b128 v[210:213], v175 offset:49152
	ds_read_b128 v[214:217], v175 offset:50176
	ds_read_b128 v[218:221], v175 offset:51200
	ds_read_b128 v[222:225], v175 offset:52224
	ds_read_b128 v[226:229], v175 offset:53248
	ds_read_b128 v[230:233], v175 offset:54272
	ds_read_b128 v[234:237], v175 offset:55296
	ds_read_b128 v[238:241], v175 offset:56320
	s_addc_u32 s23, s27, 0
	global_load_lds_dwordx4 v[242:243], off
	v_lshl_add_u64 v[242:243], v[244:245], 0, s[8:9]
	s_mov_b32 m0, s61
	s_nop 0
	global_load_lds_dwordx4 v[242:243], off
	v_lshl_add_u64 v[242:243], s[22:23], 0, v[136:137]
	s_mov_b32 m0, s62
	s_nop 0
	global_load_lds_dwordx4 v[242:243], off
	v_lshl_add_u64 v[242:243], s[22:23], 0, v[132:133]
	s_mov_b32 m0, s63
	s_nop 0
	global_load_lds_dwordx4 v[242:243], off
	v_lshl_add_u64 v[242:243], v[246:247], 0, s[8:9]
	s_mov_b32 m0, s47
	s_nop 0
	global_load_lds_dwordx4 v[242:243], off
	v_lshl_add_u64 v[242:243], v[248:249], 0, s[8:9]
	s_mov_b32 m0, s48
	s_nop 0
	global_load_lds_dwordx4 v[242:243], off
	s_waitcnt vmcnt(8)
	s_waitcnt lgkmcnt(0)
	s_barrier
	s_setprio 1
	s_waitcnt lgkmcnt(0)
	v_mfma_f32_16x16x32_bf16 v[62:65], v[178:181], v[210:213], v[62:65]
	v_mfma_f32_16x16x32_bf16 v[58:61], v[186:189], v[210:213], v[58:61]
	v_mfma_f32_16x16x32_bf16 v[54:57], v[178:181], v[218:221], v[54:57]
	v_mfma_f32_16x16x32_bf16 v[50:53], v[186:189], v[218:221], v[50:53]
	v_mfma_f32_16x16x32_bf16 v[46:49], v[178:181], v[226:229], v[46:49]
	v_mfma_f32_16x16x32_bf16 v[42:45], v[186:189], v[226:229], v[42:45]
	v_mfma_f32_16x16x32_bf16 v[34:37], v[178:181], v[234:237], v[34:37]
	v_mfma_f32_16x16x32_bf16 v[26:29], v[186:189], v[234:237], v[26:29]
	v_mfma_f32_16x16x32_bf16 v[62:65], v[182:185], v[214:217], v[62:65]
	v_mfma_f32_16x16x32_bf16 v[58:61], v[190:193], v[214:217], v[58:61]
	v_mfma_f32_16x16x32_bf16 v[54:57], v[182:185], v[222:225], v[54:57]
	v_mfma_f32_16x16x32_bf16 v[50:53], v[190:193], v[222:225], v[50:53]
	v_mfma_f32_16x16x32_bf16 v[46:49], v[182:185], v[230:233], v[46:49]
	v_mfma_f32_16x16x32_bf16 v[42:45], v[190:193], v[230:233], v[42:45]
	v_mfma_f32_16x16x32_bf16 v[34:37], v[182:185], v[238:241], v[34:37]
	v_mfma_f32_16x16x32_bf16 v[26:29], v[190:193], v[238:241], v[26:29]
	s_setprio 0
	s_setprio 1
	v_mfma_f32_16x16x32_bf16 v[38:41], v[194:197], v[210:213], v[38:41]
	v_mfma_f32_16x16x32_bf16 v[30:33], v[202:205], v[210:213], v[30:33]
	v_mfma_f32_16x16x32_bf16 v[22:25], v[194:197], v[218:221], v[22:25]
	v_mfma_f32_16x16x32_bf16 v[18:21], v[202:205], v[218:221], v[18:21]
	v_mfma_f32_16x16x32_bf16 v[14:17], v[194:197], v[226:229], v[14:17]
	v_mfma_f32_16x16x32_bf16 v[10:13], v[202:205], v[226:229], v[10:13]
	v_mfma_f32_16x16x32_bf16 v[6:9], v[194:197], v[234:237], v[6:9]
	v_mfma_f32_16x16x32_bf16 v[2:5], v[202:205], v[234:237], v[2:5]
	v_mfma_f32_16x16x32_bf16 v[38:41], v[198:201], v[214:217], v[38:41]
	v_mfma_f32_16x16x32_bf16 v[30:33], v[206:209], v[214:217], v[30:33]
	v_mfma_f32_16x16x32_bf16 v[22:25], v[198:201], v[222:225], v[22:25]
	v_mfma_f32_16x16x32_bf16 v[18:21], v[206:209], v[222:225], v[18:21]
	v_mfma_f32_16x16x32_bf16 v[14:17], v[198:201], v[230:233], v[14:17]
	v_mfma_f32_16x16x32_bf16 v[10:13], v[206:209], v[230:233], v[10:13]
	v_mfma_f32_16x16x32_bf16 v[6:9], v[198:201], v[238:241], v[6:9]
	v_mfma_f32_16x16x32_bf16 v[2:5], v[206:209], v[238:241], v[2:5]
	s_setprio 0
	s_barrier
	s_add_i32 s66, s66, 2
	s_add_u32 s15, s15, 0x100
	s_addc_u32 s65, s65, 0
	s_cmp_gt_u32 s66, 5
	s_mov_b64 s[22:23], s[24:25]
	s_cbranch_scc0 .LBB0_491
	s_branch .Lpx_13405

; #define PG8_BAR __builtin_amdgcn_s_barrier()
; template <class Epi, class Sched, bool ALIGN_EPI = true, bool F8 = false>
; __device__ __forceinline__ void gemm_phase(PG8_LAS unsigned char* lds, const Sched& S, const Epi& E) {
;     ...
;         if constexpr (ALIGN_EPI) { if (wr == 0) PG8_BAR; }
.Lpx_13405:
	s_and_b64 vcc, exec, s[10:11]
	s_cbranch_vccz .LBB0_494
	s_barrier

; #define PG8_STAGE(bufoff, gbase, voff) do { _Pragma("unroll") for (int _i = 0; _i < 2; ++_i) \
;         __builtin_amdgcn_global_load_lds((const unsigned*)((const char*)(gbase) + (voff)[_i]), (PG8_LAS unsigned*)(lds + (bufoff) + ldsw + _i * 8192), 16, 0, 0); } while (0)
; #define PG8_WAIT_V(n) asm volatile("s_waitcnt vmcnt(" #n ")" ::: "memory")
; #define PG8_WAIT_L(n) asm volatile("s_waitcnt lgkmcnt(" #n ")" ::: "memory")
; #define PG8_BAR __builtin_amdgcn_s_barrier()
; #define PG8_SCHED __builtin_amdgcn_sched_barrier(0)
; template <class Epi, class Sched, bool ALIGN_EPI = true, bool F8 = false>
; __device__ __forceinline__ void gemm_phase(PG8_LAS unsigned char* lds, const Sched& S, const Epi& E) {
;     ...
;             PG8_LDB(B0, 0, 0); PG8_LDB(B1, 0, 1); PG8_SCHED; PG8_LDA(At, 0, 0); PG8_STAGE(PG8_SA(1, 1), a1, voffA[1]);
;             PG8_WAIT_V(8); PG8_WAIT_L(0); PG8_BAR; PG8_MMA(0, 0, At, B0); PG8_MMA(0, 1, At, B1); PG8_BAR; PG8_SCHED;
;             PG8_LDA(At, 0, 1); PG8_STAGE(PG8_SB(0, 0), b2, voffB[0]); PG8_STAGE(PG8_SB(0, 1), b2, voffB[1]); PG8_STAGE(PG8_SA(0, 0), a2, vA2[0]);
;     ...
;         for (int a = 0; a < 2; ++a)
; #pragma unroll
;             for (int b = 0; b < 2; ++b)
; #pragma unroll
;                 for (int m = 0; m < 4; ++m)
; #pragma unroll
;                     for (int n = 0; n < 2; ++n) acc[a][b][m][n] = (f32x4){0.f, 0.f, 0.f, 0.f};
.LBB0_513:
	s_mov_b32 s15, 0
	s_mov_b64 s[30:31], -1
	s_mov_b64 s[40:41], 0
.Lpkb_514:
	s_add_u32 s44, s22, s15
	ds_read_b128 v[172:175], v164
	ds_read_b128 v[176:179], v164 offset:1024
	ds_read_b128 v[180:183], v164 offset:2048
	ds_read_b128 v[184:187], v164 offset:3072
	ds_read_b128 v[188:191], v165
	ds_read_b128 v[192:195], v165 offset:1024
	ds_read_b128 v[196:199], v165 offset:2048
	ds_read_b128 v[200:203], v165 offset:3072
	s_addc_u32 s45, s23, 0
	s_add_u32 s17, s44, 0x100
	s_addc_u32 s72, s45, 0
	s_and_b64 s[42:43], s[40:41], exec
	s_cselect_b32 s42, s24, s17
	s_cselect_b32 s43, s25, s72
	s_add_u32 s15, s26, s15
	s_addc_u32 s17, s27, 0
	s_add_u32 s15, s15, 0x100
	s_addc_u32 s17, s17, 0
	s_and_b64 s[40:41], s[40:41], exec
	s_cselect_b32 s40, s20, s15
	s_cselect_b32 s41, s21, s17
	v_lshl_add_u64 v[236:237], s[44:45], 0, v[142:143]
	s_mov_b32 m0, s61
	v_lshl_add_u64 v[236:237], v[236:237], 0, s[10:11]
	ds_read_b128 v[204:207], v166
	ds_read_b128 v[208:211], v166 offset:1024
	ds_read_b128 v[212:215], v166 offset:2048
	ds_read_b128 v[216:219], v166 offset:3072
	ds_read_b128 v[220:223], v166 offset:4096
	ds_read_b128 v[224:227], v166 offset:5120
	ds_read_b128 v[228:231], v166 offset:6144
	ds_read_b128 v[232:235], v166 offset:7168
	global_load_lds_dwordx4 v[236:237], off
	v_lshl_add_u64 v[236:237], s[44:45], 0, v[144:145]
	v_lshl_add_u64 v[236:237], v[236:237], 0, s[10:11]
	s_mov_b32 m0, s62
	s_nop 0
	global_load_lds_dwordx4 v[236:237], off
	s_waitcnt vmcnt(8)
	s_waitcnt lgkmcnt(0)
	s_barrier
	s_setprio 1
	s_waitcnt lgkmcnt(0)
	v_mfma_f32_16x16x32_bf16 v[126:129], v[172:175], v[204:207], 0
	v_mfma_f32_16x16x32_bf16 v[122:125], v[180:183], v[204:207], 0
	v_mfma_f32_16x16x32_bf16 v[118:121], v[172:175], v[212:215], 0
	v_mfma_f32_16x16x32_bf16 v[114:117], v[180:183], v[212:215], 0
	v_mfma_f32_16x16x32_bf16 v[102:105], v[172:175], v[220:223], 0
	v_mfma_f32_16x16x32_bf16 v[98:101], v[180:183], v[220:223], 0
	v_mfma_f32_16x16x32_bf16 v[86:89], v[172:175], v[228:231], 0
	v_mfma_f32_16x16x32_bf16 v[82:85], v[180:183], v[228:231], 0
	v_mfma_f32_16x16x32_bf16 v[126:129], v[176:179], v[208:211], v[126:129]
	v_mfma_f32_16x16x32_bf16 v[122:125], v[184:187], v[208:211], v[122:125]
	v_mfma_f32_16x16x32_bf16 v[118:121], v[176:179], v[216:219], v[118:121]
	v_mfma_f32_16x16x32_bf16 v[114:117], v[184:187], v[216:219], v[114:117]
	v_mfma_f32_16x16x32_bf16 v[102:105], v[176:179], v[224:227], v[102:105]
	v_mfma_f32_16x16x32_bf16 v[98:101], v[184:187], v[224:227], v[98:101]
	v_mfma_f32_16x16x32_bf16 v[86:89], v[176:179], v[232:235], v[86:89]
	v_mfma_f32_16x16x32_bf16 v[82:85], v[184:187], v[232:235], v[82:85]
	s_setprio 0
	s_setprio 1
	v_mfma_f32_16x16x32_bf16 v[110:113], v[188:191], v[204:207], 0
	v_mfma_f32_16x16x32_bf16 v[106:109], v[196:199], v[204:207], 0
	v_mfma_f32_16x16x32_bf16 v[94:97], v[188:191], v[212:215], 0
	v_mfma_f32_16x16x32_bf16 v[90:93], v[196:199], v[212:215], 0
	v_mfma_f32_16x16x32_bf16 v[78:81], v[188:191], v[220:223], 0
	v_mfma_f32_16x16x32_bf16 v[74:77], v[196:199], v[220:223], 0
	v_mfma_f32_16x16x32_bf16 v[70:73], v[188:191], v[228:231], 0
	v_mfma_f32_16x16x32_bf16 v[66:69], v[196:199], v[228:231], 0
	v_mfma_f32_16x16x32_bf16 v[110:113], v[192:195], v[208:211], v[110:113]
	v_mfma_f32_16x16x32_bf16 v[106:109], v[200:203], v[208:211], v[106:109]
	v_mfma_f32_16x16x32_bf16 v[94:97], v[192:195], v[216:219], v[94:97]
	v_mfma_f32_16x16x32_bf16 v[90:93], v[200:203], v[216:219], v[90:93]
	v_mfma_f32_16x16x32_bf16 v[78:81], v[192:195], v[224:227], v[78:81]
	v_mfma_f32_16x16x32_bf16 v[74:77], v[200:203], v[224:227], v[74:77]
	v_mfma_f32_16x16x32_bf16 v[70:73], v[192:195], v[232:235], v[70:73]
	v_mfma_f32_16x16x32_bf16 v[66:69], v[200:203], v[232:235], v[66:69]
	s_setprio 0
	s_barrier
	s_mov_b32 m0, s63
	v_lshl_add_u64 v[236:237], s[40:41], 0, v[136:137]
	ds_read_b128 v[204:207], v166 offset:16384
	ds_read_b128 v[208:211], v166 offset:17408
	ds_read_b128 v[212:215], v166 offset:18432
	ds_read_b128 v[216:219], v166 offset:19456
	ds_read_b128 v[220:223], v166 offset:20480
	ds_read_b128 v[224:227], v166 offset:21504
	ds_read_b128 v[228:231], v166 offset:22528
	ds_read_b128 v[232:235], v166 offset:23552
	global_load_lds_dwordx4 v[236:237], off
	v_lshl_add_u64 v[238:239], s[40:41], 0, v[134:135]
	s_mov_b32 m0, s64
	v_lshl_add_u64 v[240:241], s[40:41], 0, v[132:133]
	global_load_lds_dwordx4 v[238:239], off
	s_mov_b32 m0, s65
	v_lshl_add_u64 v[242:243], s[40:41], 0, v[130:131]
	global_load_lds_dwordx4 v[240:241], off
	s_mov_b32 m0, s66
	v_lshl_add_u64 v[244:245], s[42:43], 0, v[138:139]
	global_load_lds_dwordx4 v[242:243], off
	s_mov_b32 m0, s50
	v_lshl_add_u64 v[246:247], s[42:43], 0, v[140:141]
	global_load_lds_dwordx4 v[244:245], off
	s_mov_b32 m0, s51
	s_nop 0
	global_load_lds_dwordx4 v[246:247], off
	s_waitcnt vmcnt(8)
	s_waitcnt lgkmcnt(0)
	s_barrier
; #define PG8_STAGE(bufoff, gbase, voff) do { _Pragma("unroll") for (int _i = 0; _i < 2; ++_i) \
;         __builtin_amdgcn_global_load_lds((const unsigned*)((const char*)(gbase) + (voff)[_i]), (PG8_LAS unsigned*)(lds + (bufoff) + ldsw + _i * 8192), 16, 0, 0); } while (0)
; #define PG8_WAIT_V(n) asm volatile("s_waitcnt vmcnt(" #n ")" ::: "memory")
; #define PG8_WAIT_L(n) asm volatile("s_waitcnt lgkmcnt(" #n ")" ::: "memory")
; #define PG8_BAR __builtin_amdgcn_s_barrier()
; #define PG8_SCHED __builtin_amdgcn_sched_barrier(0)
; template <class Epi, class Sched, bool ALIGN_EPI = true, bool F8 = false>
; __device__ __forceinline__ void gemm_phase(PG8_LAS unsigned char* lds, const Sched& S, const Epi& E) {
;     ...
;             PG8_WAIT_V(8); PG8_WAIT_L(0); PG8_BAR; PG8_MMA(1, 0, At, B0); PG8_MMA(1, 1, At, B1); PG8_BAR; PG8_SCHED;
;             PG8_LDB(B0, 1, 0); PG8_LDB(B1, 1, 1); PG8_SCHED; PG8_LDA(At, 1, 0); PG8_STAGE(PG8_SA(0, 1), a2, vA2[1]);
;             PG8_WAIT_V(8); PG8_WAIT_L(0); PG8_BAR; PG8_MMA(0, 0, At, B0); PG8_MMA(0, 1, At, B1); PG8_BAR; PG8_SCHED;
	s_setprio 1
	s_waitcnt lgkmcnt(0)
	v_mfma_f32_16x16x32_bf16 v[62:65], v[172:175], v[204:207], 0
	v_mfma_f32_16x16x32_bf16 v[58:61], v[180:183], v[204:207], 0
	v_mfma_f32_16x16x32_bf16 v[54:57], v[172:175], v[212:215], 0
	v_mfma_f32_16x16x32_bf16 v[50:53], v[180:183], v[212:215], 0
	v_mfma_f32_16x16x32_bf16 v[38:41], v[172:175], v[220:223], 0
	v_mfma_f32_16x16x32_bf16 v[34:37], v[180:183], v[220:223], 0
	v_mfma_f32_16x16x32_bf16 v[22:25], v[172:175], v[228:231], 0
	v_mfma_f32_16x16x32_bf16 v[18:21], v[180:183], v[228:231], 0
	v_mfma_f32_16x16x32_bf16 v[62:65], v[176:179], v[208:211], v[62:65]
	v_mfma_f32_16x16x32_bf16 v[58:61], v[184:187], v[208:211], v[58:61]
	v_mfma_f32_16x16x32_bf16 v[54:57], v[176:179], v[216:219], v[54:57]
	v_mfma_f32_16x16x32_bf16 v[50:53], v[184:187], v[216:219], v[50:53]
	v_mfma_f32_16x16x32_bf16 v[38:41], v[176:179], v[224:227], v[38:41]
	v_mfma_f32_16x16x32_bf16 v[34:37], v[184:187], v[224:227], v[34:37]
	v_mfma_f32_16x16x32_bf16 v[22:25], v[176:179], v[232:235], v[22:25]
	v_mfma_f32_16x16x32_bf16 v[18:21], v[184:187], v[232:235], v[18:21]
	s_setprio 0
	s_setprio 1
	v_mfma_f32_16x16x32_bf16 v[46:49], v[188:191], v[204:207], 0
	v_mfma_f32_16x16x32_bf16 v[42:45], v[196:199], v[204:207], 0
	v_mfma_f32_16x16x32_bf16 v[30:33], v[188:191], v[212:215], 0
	v_mfma_f32_16x16x32_bf16 v[26:29], v[196:199], v[212:215], 0
	v_mfma_f32_16x16x32_bf16 v[14:17], v[188:191], v[220:223], 0
	v_mfma_f32_16x16x32_bf16 v[10:13], v[196:199], v[220:223], 0
	v_mfma_f32_16x16x32_bf16 v[6:9], v[188:191], v[228:231], 0
	v_mfma_f32_16x16x32_bf16 v[2:5], v[196:199], v[228:231], 0
	v_mfma_f32_16x16x32_bf16 v[46:49], v[192:195], v[208:211], v[46:49]
	v_mfma_f32_16x16x32_bf16 v[42:45], v[200:203], v[208:211], v[42:45]
	v_mfma_f32_16x16x32_bf16 v[30:33], v[192:195], v[216:219], v[30:33]
	v_mfma_f32_16x16x32_bf16 v[26:29], v[200:203], v[216:219], v[26:29]
	v_mfma_f32_16x16x32_bf16 v[14:17], v[192:195], v[224:227], v[14:17]
	v_mfma_f32_16x16x32_bf16 v[10:13], v[200:203], v[224:227], v[10:13]
	v_mfma_f32_16x16x32_bf16 v[6:9], v[192:195], v[232:235], v[6:9]
	v_mfma_f32_16x16x32_bf16 v[2:5], v[200:203], v[232:235], v[2:5]
	s_setprio 0
	s_barrier
	ds_read_b128 v[172:175], v167
	ds_read_b128 v[176:179], v167 offset:1024
	ds_read_b128 v[180:183], v167 offset:2048
	ds_read_b128 v[184:187], v167 offset:3072
	ds_read_b128 v[188:191], v168
	ds_read_b128 v[192:195], v168 offset:1024
	ds_read_b128 v[196:199], v168 offset:2048
	ds_read_b128 v[200:203], v168 offset:3072
	s_mov_b32 m0, s52
	v_lshl_add_u64 v[248:249], s[42:43], 0, v[142:143]
	ds_read_b128 v[204:207], v166 offset:32768
	ds_read_b128 v[208:211], v166 offset:33792
	ds_read_b128 v[212:215], v166 offset:34816
	ds_read_b128 v[216:219], v166 offset:35840
	ds_read_b128 v[220:223], v166 offset:36864
	ds_read_b128 v[224:227], v166 offset:37888
	ds_read_b128 v[228:231], v166 offset:38912
	ds_read_b128 v[232:235], v166 offset:39936
	global_load_lds_dwordx4 v[248:249], off
	v_lshl_add_u64 v[248:249], s[42:43], 0, v[144:145]
	s_mov_b32 m0, s53
	s_nop 0
	global_load_lds_dwordx4 v[248:249], off
	s_waitcnt vmcnt(8)
	s_waitcnt lgkmcnt(0)
	s_barrier
	s_setprio 1
	s_waitcnt lgkmcnt(0)
	v_mfma_f32_16x16x32_bf16 v[126:129], v[172:175], v[204:207], v[126:129]
	v_mfma_f32_16x16x32_bf16 v[122:125], v[180:183], v[204:207], v[122:125]
	v_mfma_f32_16x16x32_bf16 v[118:121], v[172:175], v[212:215], v[118:121]
	v_mfma_f32_16x16x32_bf16 v[114:117], v[180:183], v[212:215], v[114:117]
	v_mfma_f32_16x16x32_bf16 v[102:105], v[172:175], v[220:223], v[102:105]
	v_mfma_f32_16x16x32_bf16 v[98:101], v[180:183], v[220:223], v[98:101]
	v_mfma_f32_16x16x32_bf16 v[86:89], v[172:175], v[228:231], v[86:89]
	v_mfma_f32_16x16x32_bf16 v[82:85], v[180:183], v[228:231], v[82:85]
	v_mfma_f32_16x16x32_bf16 v[126:129], v[176:179], v[208:211], v[126:129]
	v_mfma_f32_16x16x32_bf16 v[122:125], v[184:187], v[208:211], v[122:125]
	v_mfma_f32_16x16x32_bf16 v[118:121], v[176:179], v[216:219], v[118:121]
	v_mfma_f32_16x16x32_bf16 v[114:117], v[184:187], v[216:219], v[114:117]
	v_mfma_f32_16x16x32_bf16 v[102:105], v[176:179], v[224:227], v[102:105]
	v_mfma_f32_16x16x32_bf16 v[98:101], v[184:187], v[224:227], v[98:101]
	v_mfma_f32_16x16x32_bf16 v[86:89], v[176:179], v[232:235], v[86:89]
	v_mfma_f32_16x16x32_bf16 v[82:85], v[184:187], v[232:235], v[82:85]
	s_setprio 0
	s_setprio 1
	v_mfma_f32_16x16x32_bf16 v[110:113], v[188:191], v[204:207], v[110:113]
	v_mfma_f32_16x16x32_bf16 v[106:109], v[196:199], v[204:207], v[106:109]
	v_mfma_f32_16x16x32_bf16 v[94:97], v[188:191], v[212:215], v[94:97]
	v_mfma_f32_16x16x32_bf16 v[90:93], v[196:199], v[212:215], v[90:93]
	v_mfma_f32_16x16x32_bf16 v[78:81], v[188:191], v[220:223], v[78:81]
	v_mfma_f32_16x16x32_bf16 v[74:77], v[196:199], v[220:223], v[74:77]
	v_mfma_f32_16x16x32_bf16 v[70:73], v[188:191], v[228:231], v[70:73]
	v_mfma_f32_16x16x32_bf16 v[66:69], v[196:199], v[228:231], v[66:69]
	v_mfma_f32_16x16x32_bf16 v[110:113], v[192:195], v[208:211], v[110:113]
	v_mfma_f32_16x16x32_bf16 v[106:109], v[200:203], v[208:211], v[106:109]
	v_mfma_f32_16x16x32_bf16 v[94:97], v[192:195], v[216:219], v[94:97]
	v_mfma_f32_16x16x32_bf16 v[90:93], v[200:203], v[216:219], v[90:93]
	v_mfma_f32_16x16x32_bf16 v[78:81], v[192:195], v[224:227], v[78:81]
	v_mfma_f32_16x16x32_bf16 v[74:77], v[200:203], v[224:227], v[74:77]
	v_mfma_f32_16x16x32_bf16 v[70:73], v[192:195], v[232:235], v[70:73]
	v_mfma_f32_16x16x32_bf16 v[66:69], v[200:203], v[232:235], v[66:69]
	s_setprio 0
	s_barrier
; #define PG8_STAGE(bufoff, gbase, voff) do { _Pragma("unroll") for (int _i = 0; _i < 2; ++_i) \
;         __builtin_amdgcn_global_load_lds((const unsigned*)((const char*)(gbase) + (voff)[_i]), (PG8_LAS unsigned*)(lds + (bufoff) + ldsw + _i * 8192), 16, 0, 0); } while (0)
; #define PG8_WAIT_V(n) asm volatile("s_waitcnt vmcnt(" #n ")" ::: "memory")
; #define PG8_WAIT_L(n) asm volatile("s_waitcnt lgkmcnt(" #n ")" ::: "memory")
; #define PG8_BAR __builtin_amdgcn_s_barrier()
; #define PG8_SCHED __builtin_amdgcn_sched_barrier(0)
; template <class Epi, class Sched, bool ALIGN_EPI = true, bool F8 = false>
; __device__ __forceinline__ void gemm_phase(PG8_LAS unsigned char* lds, const Sched& S, const Epi& E) {
;     ...
;         for (int t = 0; t < nt; t += 2) {
;     ...
;             PG8_LDA(At, 1, 1); PG8_STAGE(PG8_SB(1, 0), b3, voffB[0]); PG8_STAGE(PG8_SB(1, 1), b3, voffB[1]); PG8_STAGE(PG8_SA(1, 0), a3, vA2[0]);
;             PG8_WAIT_V(8); PG8_WAIT_L(0); PG8_BAR; PG8_MMA(1, 0, At, B0); PG8_MMA(1, 1, At, B1); PG8_BAR; PG8_SCHED;
	s_mov_b32 m0, s67
	v_lshl_add_u64 v[236:237], v[236:237], 0, s[10:11]
	ds_read_b128 v[204:207], v166 offset:49152
	ds_read_b128 v[208:211], v166 offset:50176
	ds_read_b128 v[212:215], v166 offset:51200
	ds_read_b128 v[216:219], v166 offset:52224
	ds_read_b128 v[220:223], v166 offset:53248
	ds_read_b128 v[224:227], v166 offset:54272
	ds_read_b128 v[228:231], v166 offset:55296
	ds_read_b128 v[232:235], v166 offset:56320
	global_load_lds_dwordx4 v[236:237], off
	v_lshl_add_u64 v[236:237], v[238:239], 0, s[10:11]
	s_mov_b32 m0, s68
	s_nop 0
	global_load_lds_dwordx4 v[236:237], off
	v_lshl_add_u64 v[236:237], v[240:241], 0, s[10:11]
	s_mov_b32 m0, s69
	s_nop 0
	global_load_lds_dwordx4 v[236:237], off
	v_lshl_add_u64 v[236:237], v[242:243], 0, s[10:11]
	s_mov_b32 m0, s70
	s_nop 0
	global_load_lds_dwordx4 v[236:237], off
	v_lshl_add_u64 v[236:237], v[244:245], 0, s[10:11]
	s_mov_b32 m0, s59
	s_nop 0
	global_load_lds_dwordx4 v[236:237], off
	v_lshl_add_u64 v[236:237], v[246:247], 0, s[10:11]
	s_mov_b32 m0, s60
	s_nop 0
	global_load_lds_dwordx4 v[236:237], off
	s_waitcnt vmcnt(8)
	s_waitcnt lgkmcnt(0)
	s_barrier
	s_setprio 1
	s_waitcnt lgkmcnt(0)
	v_mfma_f32_16x16x32_bf16 v[62:65], v[172:175], v[204:207], v[62:65]
	v_mfma_f32_16x16x32_bf16 v[58:61], v[180:183], v[204:207], v[58:61]
	v_mfma_f32_16x16x32_bf16 v[54:57], v[172:175], v[212:215], v[54:57]
	v_mfma_f32_16x16x32_bf16 v[50:53], v[180:183], v[212:215], v[50:53]
	v_mfma_f32_16x16x32_bf16 v[38:41], v[172:175], v[220:223], v[38:41]
	v_mfma_f32_16x16x32_bf16 v[34:37], v[180:183], v[220:223], v[34:37]
	v_mfma_f32_16x16x32_bf16 v[22:25], v[172:175], v[228:231], v[22:25]
	v_mfma_f32_16x16x32_bf16 v[18:21], v[180:183], v[228:231], v[18:21]
	v_mfma_f32_16x16x32_bf16 v[62:65], v[176:179], v[208:211], v[62:65]
	v_mfma_f32_16x16x32_bf16 v[58:61], v[184:187], v[208:211], v[58:61]
	v_mfma_f32_16x16x32_bf16 v[54:57], v[176:179], v[216:219], v[54:57]
	v_mfma_f32_16x16x32_bf16 v[50:53], v[184:187], v[216:219], v[50:53]
	v_mfma_f32_16x16x32_bf16 v[38:41], v[176:179], v[224:227], v[38:41]
	v_mfma_f32_16x16x32_bf16 v[34:37], v[184:187], v[224:227], v[34:37]
	v_mfma_f32_16x16x32_bf16 v[22:25], v[176:179], v[232:235], v[22:25]
	v_mfma_f32_16x16x32_bf16 v[18:21], v[184:187], v[232:235], v[18:21]
	s_setprio 0
	s_setprio 1
	v_mfma_f32_16x16x32_bf16 v[46:49], v[188:191], v[204:207], v[46:49]
	v_mfma_f32_16x16x32_bf16 v[42:45], v[196:199], v[204:207], v[42:45]
	v_mfma_f32_16x16x32_bf16 v[30:33], v[188:191], v[212:215], v[30:33]
	v_mfma_f32_16x16x32_bf16 v[26:29], v[196:199], v[212:215], v[26:29]
	v_mfma_f32_16x16x32_bf16 v[14:17], v[188:191], v[220:223], v[14:17]
	v_mfma_f32_16x16x32_bf16 v[10:13], v[196:199], v[220:223], v[10:13]
	v_mfma_f32_16x16x32_bf16 v[6:9], v[188:191], v[228:231], v[6:9]
	v_mfma_f32_16x16x32_bf16 v[2:5], v[196:199], v[228:231], v[2:5]
	v_mfma_f32_16x16x32_bf16 v[46:49], v[192:195], v[208:211], v[46:49]
	v_mfma_f32_16x16x32_bf16 v[42:45], v[200:203], v[208:211], v[42:45]
	v_mfma_f32_16x16x32_bf16 v[30:33], v[192:195], v[216:219], v[30:33]
	v_mfma_f32_16x16x32_bf16 v[26:29], v[200:203], v[216:219], v[26:29]
	v_mfma_f32_16x16x32_bf16 v[14:17], v[192:195], v[224:227], v[14:17]
	v_mfma_f32_16x16x32_bf16 v[10:13], v[200:203], v[224:227], v[10:13]
	v_mfma_f32_16x16x32_bf16 v[6:9], v[192:195], v[232:235], v[6:9]
	v_mfma_f32_16x16x32_bf16 v[2:5], v[200:203], v[232:235], v[2:5]
	s_setprio 0
	s_barrier
	s_movk_i32 s15, 0x100
	s_andn2_b64 vcc, exec, s[30:31]
	s_mov_b64 s[40:41], -1
	s_mov_b64 s[30:31], 0
	s_cbranch_vccz .LBB0_514
	s_branch .Lpx_14299

; #define PG8_BAR __builtin_amdgcn_s_barrier()
; template <class Epi, class Sched, bool ALIGN_EPI = true, bool F8 = false>
; __device__ __forceinline__ void gemm_phase(PG8_LAS unsigned char* lds, const Sched& S, const Epi& E) {
;     ...
;         if constexpr (ALIGN_EPI) { if (wr == 0) PG8_BAR; }
.Lpx_14299:
	s_and_b64 vcc, exec, s[12:13]
	s_cbranch_vccz .LBB0_517
	s_barrier

; #define PG8_STAGE(bufoff, gbase, voff) do { _Pragma("unroll") for (int _i = 0; _i < 2; ++_i) \
;         __builtin_amdgcn_global_load_lds((const unsigned*)((const char*)(gbase) + (voff)[_i]), (PG8_LAS unsigned*)(lds + (bufoff) + ldsw + _i * 8192), 16, 0, 0); } while (0)
; #define PG8_WAIT_V(n) asm volatile("s_waitcnt vmcnt(" #n ")" ::: "memory")
; #define PG8_WAIT_L(n) asm volatile("s_waitcnt lgkmcnt(" #n ")" ::: "memory")
; #define PG8_BAR __builtin_amdgcn_s_barrier()
; #define PG8_SCHED __builtin_amdgcn_sched_barrier(0)
; template <class Epi, class Sched, bool ALIGN_EPI = true, bool F8 = false>
; __device__ __forceinline__ void gemm_phase(PG8_LAS unsigned char* lds, const Sched& S, const Epi& E) {
;     ...
;             PG8_LDB(B0, 0, 0); PG8_LDB(B1, 0, 1); PG8_SCHED; PG8_LDA(At, 0, 0); PG8_STAGE(PG8_SA(1, 1), a1, voffA[1]);
;             PG8_WAIT_V(8); PG8_WAIT_L(0); PG8_BAR; PG8_MMA(0, 0, At, B0); PG8_MMA(0, 1, At, B1); PG8_BAR; PG8_SCHED;
;             PG8_LDA(At, 0, 1); PG8_STAGE(PG8_SB(0, 0), b2, voffB[0]); PG8_STAGE(PG8_SB(0, 1), b2, voffB[1]); PG8_STAGE(PG8_SA(0, 0), a2, vA2[0]);
;             PG8_WAIT_V(8); PG8_WAIT_L(0); PG8_BAR; PG8_MMA(1, 0, At, B0); PG8_MMA(1, 1, At, B1); PG8_BAR; PG8_SCHED;
;     ...
;         for (int a = 0; a < 2; ++a)
; #pragma unroll
;             for (int b = 0; b < 2; ++b)
; #pragma unroll
;                 for (int m = 0; m < 4; ++m)
; #pragma unroll
;                     for (int n = 0; n < 2; ++n) acc[a][b][m][n] = (f32x4){0.f, 0.f, 0.f, 0.f};
.LBB0_675:
	s_add_u32 s63, s22, 0x100
	s_addc_u32 s64, s23, 0
	s_mov_b32 s65, -2
.Lpkb_676:
	ds_read_b128 v[180:183], v174
	ds_read_b128 v[184:187], v174 offset:1024
	ds_read_b128 v[188:191], v174 offset:2048
	ds_read_b128 v[192:195], v174 offset:3072
	ds_read_b128 v[196:199], v175
	ds_read_b128 v[200:203], v175 offset:1024
	ds_read_b128 v[204:207], v175 offset:2048
	ds_read_b128 v[208:211], v175 offset:3072
	s_add_u32 s22, s20, 0x100
	s_addc_u32 s23, s21, 0
	s_cmp_eq_u32 s65, 8
	s_cselect_b32 s25, s13, s23
	s_cselect_b32 s24, s12, s22
	s_cselect_b32 s67, s15, s64
	s_cselect_b32 s66, s14, s63
	s_mov_b32 m0, s45
	v_lshl_add_u64 v[166:167], s[20:21], 0, v[164:165]
	ds_read_b128 v[212:215], v176
	ds_read_b128 v[216:219], v176 offset:1024
	ds_read_b128 v[220:223], v176 offset:2048
	ds_read_b128 v[224:227], v176 offset:3072
	ds_read_b128 v[228:231], v176 offset:4096
	ds_read_b128 v[232:235], v176 offset:5120
	ds_read_b128 v[236:239], v176 offset:6144
	ds_read_b128 v[240:243], v176 offset:7168
	global_load_lds_dwordx4 v[166:167], off
	v_lshl_add_u64 v[166:167], s[20:21], 0, v[162:163]
	s_mov_b32 m0, s46
	s_nop 0
	global_load_lds_dwordx4 v[166:167], off
	s_waitcnt vmcnt(8)
	s_waitcnt lgkmcnt(0)
	s_barrier
	s_setprio 1
	s_waitcnt lgkmcnt(0)
	v_mfma_f32_16x16x32_bf16 v[126:129], v[180:183], v[212:215], 0
	v_mfma_f32_16x16x32_bf16 v[122:125], v[188:191], v[212:215], 0
	v_mfma_f32_16x16x32_bf16 v[110:113], v[180:183], v[220:223], 0
	v_mfma_f32_16x16x32_bf16 v[106:109], v[188:191], v[220:223], 0
	v_mfma_f32_16x16x32_bf16 v[94:97], v[180:183], v[228:231], 0
	v_mfma_f32_16x16x32_bf16 v[90:93], v[188:191], v[228:231], 0
	v_mfma_f32_16x16x32_bf16 v[78:81], v[180:183], v[236:239], 0
	v_mfma_f32_16x16x32_bf16 v[74:77], v[188:191], v[236:239], 0
	v_mfma_f32_16x16x32_bf16 v[126:129], v[184:187], v[216:219], v[126:129]
	v_mfma_f32_16x16x32_bf16 v[122:125], v[192:195], v[216:219], v[122:125]
	v_mfma_f32_16x16x32_bf16 v[110:113], v[184:187], v[224:227], v[110:113]
	v_mfma_f32_16x16x32_bf16 v[106:109], v[192:195], v[224:227], v[106:109]
	v_mfma_f32_16x16x32_bf16 v[94:97], v[184:187], v[232:235], v[94:97]
	v_mfma_f32_16x16x32_bf16 v[90:93], v[192:195], v[232:235], v[90:93]
	v_mfma_f32_16x16x32_bf16 v[78:81], v[184:187], v[240:243], v[78:81]
	v_mfma_f32_16x16x32_bf16 v[74:77], v[192:195], v[240:243], v[74:77]
	s_setprio 0
	s_setprio 1
	v_mfma_f32_16x16x32_bf16 v[118:121], v[196:199], v[212:215], 0
	v_mfma_f32_16x16x32_bf16 v[114:117], v[204:207], v[212:215], 0
	v_mfma_f32_16x16x32_bf16 v[102:105], v[196:199], v[220:223], 0
	v_mfma_f32_16x16x32_bf16 v[98:101], v[204:207], v[220:223], 0
	v_mfma_f32_16x16x32_bf16 v[86:89], v[196:199], v[228:231], 0
	v_mfma_f32_16x16x32_bf16 v[82:85], v[204:207], v[228:231], 0
	v_mfma_f32_16x16x32_bf16 v[70:73], v[196:199], v[236:239], 0
	v_mfma_f32_16x16x32_bf16 v[66:69], v[204:207], v[236:239], 0
	v_mfma_f32_16x16x32_bf16 v[118:121], v[200:203], v[216:219], v[118:121]
	v_mfma_f32_16x16x32_bf16 v[114:117], v[208:211], v[216:219], v[114:117]
	v_mfma_f32_16x16x32_bf16 v[102:105], v[200:203], v[224:227], v[102:105]
	v_mfma_f32_16x16x32_bf16 v[98:101], v[208:211], v[224:227], v[98:101]
	v_mfma_f32_16x16x32_bf16 v[86:89], v[200:203], v[232:235], v[86:89]
	v_mfma_f32_16x16x32_bf16 v[82:85], v[208:211], v[232:235], v[82:85]
	v_mfma_f32_16x16x32_bf16 v[70:73], v[200:203], v[240:243], v[70:73]
	v_mfma_f32_16x16x32_bf16 v[66:69], v[208:211], v[240:243], v[66:69]
	s_setprio 0
	s_barrier
	s_mov_b32 m0, s47
	v_lshl_add_u64 v[166:167], s[66:67], 0, v[134:135]
	ds_read_b128 v[212:215], v176 offset:16384
	ds_read_b128 v[216:219], v176 offset:17408
	ds_read_b128 v[220:223], v176 offset:18432
	ds_read_b128 v[224:227], v176 offset:19456
	ds_read_b128 v[228:231], v176 offset:20480
	ds_read_b128 v[232:235], v176 offset:21504
	ds_read_b128 v[236:239], v176 offset:22528
	ds_read_b128 v[240:243], v176 offset:23552
	global_load_lds_dwordx4 v[166:167], off
	v_lshl_add_u64 v[244:245], s[66:67], 0, v[130:131]
	s_mov_b32 m0, s48
	v_lshl_add_u64 v[246:247], s[66:67], 0, v[136:137]
	global_load_lds_dwordx4 v[244:245], off
	s_mov_b32 m0, s49
	v_lshl_add_u64 v[248:249], s[66:67], 0, v[132:133]
	global_load_lds_dwordx4 v[246:247], off
	s_mov_b32 m0, s50
	v_lshl_add_u64 v[250:251], s[24:25], 0, v[138:139]
	global_load_lds_dwordx4 v[248:249], off
	s_mov_b32 m0, s30
	v_lshl_add_u64 v[252:253], s[24:25], 0, v[140:141]
	global_load_lds_dwordx4 v[250:251], off
	s_mov_b32 m0, s31
	s_nop 0
	global_load_lds_dwordx4 v[252:253], off
	s_waitcnt vmcnt(8)
	s_waitcnt lgkmcnt(0)
	s_barrier
	s_setprio 1
	s_waitcnt lgkmcnt(0)
	v_mfma_f32_16x16x32_bf16 v[62:65], v[180:183], v[212:215], 0
	v_mfma_f32_16x16x32_bf16 v[58:61], v[188:191], v[212:215], 0
	v_mfma_f32_16x16x32_bf16 v[46:49], v[180:183], v[220:223], 0
	v_mfma_f32_16x16x32_bf16 v[42:45], v[188:191], v[220:223], 0
	v_mfma_f32_16x16x32_bf16 v[30:33], v[180:183], v[228:231], 0
	v_mfma_f32_16x16x32_bf16 v[26:29], v[188:191], v[228:231], 0
	v_mfma_f32_16x16x32_bf16 v[14:17], v[180:183], v[236:239], 0
	v_mfma_f32_16x16x32_bf16 v[10:13], v[188:191], v[236:239], 0
	v_mfma_f32_16x16x32_bf16 v[62:65], v[184:187], v[216:219], v[62:65]
	v_mfma_f32_16x16x32_bf16 v[58:61], v[192:195], v[216:219], v[58:61]
	v_mfma_f32_16x16x32_bf16 v[46:49], v[184:187], v[224:227], v[46:49]
	v_mfma_f32_16x16x32_bf16 v[42:45], v[192:195], v[224:227], v[42:45]
	v_mfma_f32_16x16x32_bf16 v[30:33], v[184:187], v[232:235], v[30:33]
	v_mfma_f32_16x16x32_bf16 v[26:29], v[192:195], v[232:235], v[26:29]
	v_mfma_f32_16x16x32_bf16 v[14:17], v[184:187], v[240:243], v[14:17]
	v_mfma_f32_16x16x32_bf16 v[10:13], v[192:195], v[240:243], v[10:13]
	s_setprio 0
	s_setprio 1
	v_mfma_f32_16x16x32_bf16 v[54:57], v[196:199], v[212:215], 0
	v_mfma_f32_16x16x32_bf16 v[50:53], v[204:207], v[212:215], 0
	v_mfma_f32_16x16x32_bf16 v[38:41], v[196:199], v[220:223], 0
	v_mfma_f32_16x16x32_bf16 v[34:37], v[204:207], v[220:223], 0
	v_mfma_f32_16x16x32_bf16 v[22:25], v[196:199], v[228:231], 0
	v_mfma_f32_16x16x32_bf16 v[18:21], v[204:207], v[228:231], 0
	v_mfma_f32_16x16x32_bf16 v[6:9], v[196:199], v[236:239], 0
	v_mfma_f32_16x16x32_bf16 v[2:5], v[204:207], v[236:239], 0
	v_mfma_f32_16x16x32_bf16 v[54:57], v[200:203], v[216:219], v[54:57]
	v_mfma_f32_16x16x32_bf16 v[50:53], v[208:211], v[216:219], v[50:53]
	v_mfma_f32_16x16x32_bf16 v[38:41], v[200:203], v[224:227], v[38:41]
	v_mfma_f32_16x16x32_bf16 v[34:37], v[208:211], v[224:227], v[34:37]
	v_mfma_f32_16x16x32_bf16 v[22:25], v[200:203], v[232:235], v[22:25]
	v_mfma_f32_16x16x32_bf16 v[18:21], v[208:211], v[232:235], v[18:21]
	v_mfma_f32_16x16x32_bf16 v[6:9], v[200:203], v[240:243], v[6:9]
	v_mfma_f32_16x16x32_bf16 v[2:5], v[208:211], v[240:243], v[2:5]
	s_setprio 0
	s_barrier
; #define PG8_STAGE(bufoff, gbase, voff) do { _Pragma("unroll") for (int _i = 0; _i < 2; ++_i) \
;         __builtin_amdgcn_global_load_lds((const unsigned*)((const char*)(gbase) + (voff)[_i]), (PG8_LAS unsigned*)(lds + (bufoff) + ldsw + _i * 8192), 16, 0, 0); } while (0)
; #define PG8_WAIT_V(n) asm volatile("s_waitcnt vmcnt(" #n ")" ::: "memory")
; #define PG8_WAIT_L(n) asm volatile("s_waitcnt lgkmcnt(" #n ")" ::: "memory")
; template <class Epi, class Sched, bool ALIGN_EPI = true, bool F8 = false>
; __device__ __forceinline__ void gemm_phase(PG8_LAS unsigned char* lds, const Sched& S, const Epi& E) {
;     ...
;         for (int t = 0; t < nt; t += 2) {
;             const bool last = (t == nt - 2);
;             if constexpr (Sched::GATHER) { if (last && has_next) S.a_off(nxt, Rs, Cs, voffAn); }
;             const char* a1 = cA + (size_t)(t + 1) * kstep;
;             const char* a2 = last ? nA : cA + (size_t)(t + 2) * kstep; const char* b2 = last ? nB : cB + (size_t)(t + 2) * kstepB;
;             const char* a3 = a2 + kstep; const char* b3 = b2 + kstepB;
;             unsigned vA2[2][2];
; #pragma unroll
;             for (int h = 0; h < 2; ++h)
; #pragma unroll
;                 for (int i = 0; i < 2; ++i) { if constexpr (Sched::GATHER) vA2[h][i] = (last && has_next) ? voffAn[h][i] : voffA[h][i]; else vA2[h][i] = voffA[h][i]; }
;             PG8_LDB(B0, 0, 0); PG8_LDB(B1, 0, 1); PG8_SCHED; PG8_LDA(At, 0, 0); PG8_STAGE(PG8_SA(1, 1), a1, voffA[1]);
;             PG8_WAIT_V(8); PG8_WAIT_L(0); PG8_BAR; PG8_MMA(0, 0, At, B0); PG8_MMA(0, 1, At, B1); PG8_BAR; PG8_SCHED;
;             PG8_LDA(At, 0, 1); PG8_STAGE(PG8_SB(0, 0), b2, voffB[0]); PG8_STAGE(PG8_SB(0, 1), b2, voffB[1]); PG8_STAGE(PG8_SA(0, 0), a2, vA2[0]);
;             PG8_WAIT_V(8); PG8_WAIT_L(0); PG8_BAR; PG8_MMA(1, 0, At, B0); PG8_MMA(1, 1, At, B1); PG8_BAR; PG8_SCHED;
;             PG8_LDB(B0, 1, 0); PG8_LDB(B1, 1, 1); PG8_SCHED; PG8_LDA(At, 1, 0); PG8_STAGE(PG8_SA(0, 1), a2, vA2[1]);
;             PG8_WAIT_V(8); PG8_WAIT_L(0); PG8_BAR; PG8_MMA(0, 0, At, B0); PG8_MMA(0, 1, At, B1); PG8_BAR; PG8_SCHED;
;             PG8_LDA(At, 1, 1); PG8_STAGE(PG8_SB(1, 0), b3, voffB[0]); PG8_STAGE(PG8_SB(1, 1), b3, voffB[1]); PG8_STAGE(PG8_SA(1, 0), a3, vA2[0]);
;             PG8_WAIT_V(8); PG8_WAIT_L(0); PG8_BAR; PG8_MMA(1, 0, At, B0); PG8_MMA(1, 1, At, B1); PG8_BAR; PG8_SCHED;
	ds_read_b128 v[180:183], v177
	ds_read_b128 v[184:187], v177 offset:1024
	ds_read_b128 v[188:191], v177 offset:2048
	ds_read_b128 v[192:195], v177 offset:3072
	ds_read_b128 v[196:199], v178
	ds_read_b128 v[200:203], v178 offset:1024
	ds_read_b128 v[204:207], v178 offset:2048
	ds_read_b128 v[208:211], v178 offset:3072
	s_mov_b32 m0, s40
	v_lshl_add_u64 v[254:255], s[24:25], 0, v[142:143]
	ds_read_b128 v[212:215], v176 offset:32768
	ds_read_b128 v[216:219], v176 offset:33792
	ds_read_b128 v[220:223], v176 offset:34816
	ds_read_b128 v[224:227], v176 offset:35840
	ds_read_b128 v[228:231], v176 offset:36864
	ds_read_b128 v[232:235], v176 offset:37888
	ds_read_b128 v[236:239], v176 offset:38912
	ds_read_b128 v[240:243], v176 offset:39936
	global_load_lds_dwordx4 v[254:255], off
	v_lshl_add_u64 v[254:255], s[24:25], 0, v[144:145]
	s_mov_b32 m0, s41
	s_nop 0
	global_load_lds_dwordx4 v[254:255], off
	s_waitcnt vmcnt(8)
	s_waitcnt lgkmcnt(0)
	s_barrier
	s_setprio 1
	s_waitcnt lgkmcnt(0)
	v_mfma_f32_16x16x32_bf16 v[126:129], v[180:183], v[212:215], v[126:129]
	v_mfma_f32_16x16x32_bf16 v[122:125], v[188:191], v[212:215], v[122:125]
	v_mfma_f32_16x16x32_bf16 v[110:113], v[180:183], v[220:223], v[110:113]
	v_mfma_f32_16x16x32_bf16 v[106:109], v[188:191], v[220:223], v[106:109]
	v_mfma_f32_16x16x32_bf16 v[94:97], v[180:183], v[228:231], v[94:97]
	v_mfma_f32_16x16x32_bf16 v[90:93], v[188:191], v[228:231], v[90:93]
	v_mfma_f32_16x16x32_bf16 v[78:81], v[180:183], v[236:239], v[78:81]
	v_mfma_f32_16x16x32_bf16 v[74:77], v[188:191], v[236:239], v[74:77]
	v_mfma_f32_16x16x32_bf16 v[126:129], v[184:187], v[216:219], v[126:129]
	v_mfma_f32_16x16x32_bf16 v[122:125], v[192:195], v[216:219], v[122:125]
	v_mfma_f32_16x16x32_bf16 v[110:113], v[184:187], v[224:227], v[110:113]
	v_mfma_f32_16x16x32_bf16 v[106:109], v[192:195], v[224:227], v[106:109]
	v_mfma_f32_16x16x32_bf16 v[94:97], v[184:187], v[232:235], v[94:97]
	v_mfma_f32_16x16x32_bf16 v[90:93], v[192:195], v[232:235], v[90:93]
	v_mfma_f32_16x16x32_bf16 v[78:81], v[184:187], v[240:243], v[78:81]
	v_mfma_f32_16x16x32_bf16 v[74:77], v[192:195], v[240:243], v[74:77]
	s_setprio 0
	s_setprio 1
	v_mfma_f32_16x16x32_bf16 v[118:121], v[196:199], v[212:215], v[118:121]
	v_mfma_f32_16x16x32_bf16 v[114:117], v[204:207], v[212:215], v[114:117]
	v_mfma_f32_16x16x32_bf16 v[102:105], v[196:199], v[220:223], v[102:105]
	v_mfma_f32_16x16x32_bf16 v[98:101], v[204:207], v[220:223], v[98:101]
	v_mfma_f32_16x16x32_bf16 v[86:89], v[196:199], v[228:231], v[86:89]
	v_mfma_f32_16x16x32_bf16 v[82:85], v[204:207], v[228:231], v[82:85]
	v_mfma_f32_16x16x32_bf16 v[70:73], v[196:199], v[236:239], v[70:73]
	v_mfma_f32_16x16x32_bf16 v[66:69], v[204:207], v[236:239], v[66:69]
	v_mfma_f32_16x16x32_bf16 v[118:121], v[200:203], v[216:219], v[118:121]
	v_mfma_f32_16x16x32_bf16 v[114:117], v[208:211], v[216:219], v[114:117]
	v_mfma_f32_16x16x32_bf16 v[102:105], v[200:203], v[224:227], v[102:105]
	v_mfma_f32_16x16x32_bf16 v[98:101], v[208:211], v[224:227], v[98:101]
	v_mfma_f32_16x16x32_bf16 v[86:89], v[200:203], v[232:235], v[86:89]
	v_mfma_f32_16x16x32_bf16 v[82:85], v[208:211], v[232:235], v[82:85]
	v_mfma_f32_16x16x32_bf16 v[70:73], v[200:203], v[240:243], v[70:73]
	v_mfma_f32_16x16x32_bf16 v[66:69], v[208:211], v[240:243], v[66:69]
	s_setprio 0
	s_barrier
	s_mov_b32 m0, s51
	v_lshl_add_u64 v[166:167], v[166:167], 0, s[8:9]
	ds_read_b128 v[212:215], v176 offset:49152
	ds_read_b128 v[216:219], v176 offset:50176
	ds_read_b128 v[220:223], v176 offset:51200
	ds_read_b128 v[224:227], v176 offset:52224
	ds_read_b128 v[228:231], v176 offset:53248
	ds_read_b128 v[232:235], v176 offset:54272
	ds_read_b128 v[236:239], v176 offset:55296
	ds_read_b128 v[240:243], v176 offset:56320
	global_load_lds_dwordx4 v[166:167], off
	v_lshl_add_u64 v[166:167], v[244:245], 0, s[8:9]
	s_mov_b32 m0, s52
	s_nop 0
	global_load_lds_dwordx4 v[166:167], off
	v_lshl_add_u64 v[166:167], v[246:247], 0, s[8:9]
	s_mov_b32 m0, s53
	s_nop 0
	global_load_lds_dwordx4 v[166:167], off
	v_lshl_add_u64 v[166:167], v[248:249], 0, s[8:9]
	s_mov_b32 m0, s58
	s_nop 0
	global_load_lds_dwordx4 v[166:167], off
	v_lshl_add_u64 v[166:167], v[250:251], 0, s[8:9]
	s_mov_b32 m0, s43
	s_nop 0
	global_load_lds_dwordx4 v[166:167], off
	v_lshl_add_u64 v[166:167], v[252:253], 0, s[8:9]
	s_mov_b32 m0, s44
	s_nop 0
	global_load_lds_dwordx4 v[166:167], off
	s_waitcnt vmcnt(8)
	s_waitcnt lgkmcnt(0)
	s_barrier
	s_setprio 1
	s_waitcnt lgkmcnt(0)
	v_mfma_f32_16x16x32_bf16 v[62:65], v[180:183], v[212:215], v[62:65]
	v_mfma_f32_16x16x32_bf16 v[58:61], v[188:191], v[212:215], v[58:61]
	v_mfma_f32_16x16x32_bf16 v[46:49], v[180:183], v[220:223], v[46:49]
	v_mfma_f32_16x16x32_bf16 v[42:45], v[188:191], v[220:223], v[42:45]
	v_mfma_f32_16x16x32_bf16 v[30:33], v[180:183], v[228:231], v[30:33]
	v_mfma_f32_16x16x32_bf16 v[26:29], v[188:191], v[228:231], v[26:29]
	v_mfma_f32_16x16x32_bf16 v[14:17], v[180:183], v[236:239], v[14:17]
	v_mfma_f32_16x16x32_bf16 v[10:13], v[188:191], v[236:239], v[10:13]
	v_mfma_f32_16x16x32_bf16 v[62:65], v[184:187], v[216:219], v[62:65]
	v_mfma_f32_16x16x32_bf16 v[58:61], v[192:195], v[216:219], v[58:61]
	v_mfma_f32_16x16x32_bf16 v[46:49], v[184:187], v[224:227], v[46:49]
	v_mfma_f32_16x16x32_bf16 v[42:45], v[192:195], v[224:227], v[42:45]
	v_mfma_f32_16x16x32_bf16 v[30:33], v[184:187], v[232:235], v[30:33]
	v_mfma_f32_16x16x32_bf16 v[26:29], v[192:195], v[232:235], v[26:29]
	v_mfma_f32_16x16x32_bf16 v[14:17], v[184:187], v[240:243], v[14:17]
	v_mfma_f32_16x16x32_bf16 v[10:13], v[192:195], v[240:243], v[10:13]
	s_setprio 0
	s_setprio 1
	v_mfma_f32_16x16x32_bf16 v[54:57], v[196:199], v[212:215], v[54:57]
	v_mfma_f32_16x16x32_bf16 v[50:53], v[204:207], v[212:215], v[50:53]
	v_mfma_f32_16x16x32_bf16 v[38:41], v[196:199], v[220:223], v[38:41]
	v_mfma_f32_16x16x32_bf16 v[34:37], v[204:207], v[220:223], v[34:37]
	v_mfma_f32_16x16x32_bf16 v[22:25], v[196:199], v[228:231], v[22:25]
	v_mfma_f32_16x16x32_bf16 v[18:21], v[204:207], v[228:231], v[18:21]
	v_mfma_f32_16x16x32_bf16 v[6:9], v[196:199], v[236:239], v[6:9]
	v_mfma_f32_16x16x32_bf16 v[2:5], v[204:207], v[236:239], v[2:5]
	v_mfma_f32_16x16x32_bf16 v[54:57], v[200:203], v[216:219], v[54:57]
	v_mfma_f32_16x16x32_bf16 v[50:53], v[208:211], v[216:219], v[50:53]
	v_mfma_f32_16x16x32_bf16 v[38:41], v[200:203], v[224:227], v[38:41]
	v_mfma_f32_16x16x32_bf16 v[34:37], v[208:211], v[224:227], v[34:37]
	v_mfma_f32_16x16x32_bf16 v[22:25], v[200:203], v[232:235], v[22:25]
	v_mfma_f32_16x16x32_bf16 v[18:21], v[208:211], v[232:235], v[18:21]
	v_mfma_f32_16x16x32_bf16 v[6:9], v[200:203], v[240:243], v[6:9]
	v_mfma_f32_16x16x32_bf16 v[2:5], v[208:211], v[240:243], v[2:5]
	s_setprio 0
	s_barrier
	s_add_i32 s65, s65, 2
	s_add_u32 s63, s63, 0x100
	s_addc_u32 s64, s64, 0
	s_cmp_gt_u32 s65, 9
	s_mov_b64 s[20:21], s[22:23]
	s_cbranch_scc0 .LBB0_676
	s_branch .Lpx_17518

; #define PG8_STAGE(bufoff, gbase, voff) do { _Pragma("unroll") for (int _i = 0; _i < 2; ++_i) \
;         __builtin_amdgcn_global_load_lds((const unsigned*)((const char*)(gbase) + (voff)[_i]), (PG8_LAS unsigned*)(lds + (bufoff) + ldsw + _i * 8192), 16, 0, 0); } while (0)
; #define PG8_WAIT_V(n) asm volatile("s_waitcnt vmcnt(" #n ")" ::: "memory")
; #define PG8_WAIT_L(n) asm volatile("s_waitcnt lgkmcnt(" #n ")" ::: "memory")
; #define PG8_BAR __builtin_amdgcn_s_barrier()
; #define PG8_SCHED __builtin_amdgcn_sched_barrier(0)
; template <class Epi, class Sched, bool ALIGN_EPI = true, bool F8 = false>
; __device__ __forceinline__ void gemm_phase(PG8_LAS unsigned char* lds, const Sched& S, const Epi& E) {
;     ...
;             PG8_LDB(B0, 0, 0); PG8_LDB(B1, 0, 1); PG8_SCHED; PG8_LDA(At, 0, 0); PG8_STAGE(PG8_SA(1, 1), a1, voffA[1]);
;             PG8_WAIT_V(8); PG8_WAIT_L(0); PG8_BAR; PG8_MMA(0, 0, At, B0); PG8_MMA(0, 1, At, B1); PG8_BAR; PG8_SCHED;
;             PG8_LDA(At, 0, 1); PG8_STAGE(PG8_SB(0, 0), b2, voffB[0]); PG8_STAGE(PG8_SB(0, 1), b2, voffB[1]); PG8_STAGE(PG8_SA(0, 0), a2, vA2[0]);
;             PG8_WAIT_V(8); PG8_WAIT_L(0); PG8_BAR; PG8_MMA(1, 0, At, B0); PG8_MMA(1, 1, At, B1); PG8_BAR; PG8_SCHED;
;     ...
;         for (int a = 0; a < 2; ++a)
; #pragma unroll
;             for (int b = 0; b < 2; ++b)
; #pragma unroll
;                 for (int m = 0; m < 4; ++m)
; #pragma unroll
;                     for (int n = 0; n < 2; ++n) acc[a][b][m][n] = (f32x4){0.f, 0.f, 0.f, 0.f};
.LBB0_691:
	s_mov_b32 s19, 0
	s_mov_b64 s[22:23], -1
	s_mov_b64 s[24:25], 0
.Lpkb_692:
	s_add_u32 s30, s4, s19
	s_addc_u32 s31, s5, 0
	s_add_i32 s28, s19, 0x100
	s_and_b64 s[26:27], s[24:25], exec
	s_cselect_b32 s26, 0, s28
	s_cselect_b32 s27, 0, 0
	s_add_u32 s26, s4, s26
	ds_read_b128 v[100:103], v94
	ds_read_b128 v[104:107], v94 offset:1024
	ds_read_b128 v[108:111], v94 offset:2048
	ds_read_b128 v[112:115], v94 offset:3072
	ds_read_b128 v[116:119], v95
	ds_read_b128 v[120:123], v95 offset:1024
	ds_read_b128 v[124:127], v95 offset:2048
	ds_read_b128 v[128:131], v95 offset:3072
	s_addc_u32 s27, s5, s27
	s_add_u32 s19, s20, s19
	s_addc_u32 s28, s21, 0
	s_add_u32 s19, s19, 0x100
	s_addc_u32 s28, s28, 0
	s_and_b64 s[24:25], s[24:25], exec
	s_cselect_b32 s29, s15, s28
	s_cselect_b32 s28, s14, s19
	s_add_u32 s30, s30, 0x80
	s_addc_u32 s31, s31, 0
	s_add_u32 s24, s28, 0x80
	s_addc_u32 s25, s29, 0
	s_mov_b32 m0, s51
	v_lshl_add_u64 v[164:165], s[30:31], 0, v[78:79]
	ds_read_b128 v[132:135], v96
	ds_read_b128 v[136:139], v96 offset:1024
	ds_read_b128 v[140:143], v96 offset:2048
	ds_read_b128 v[144:147], v96 offset:3072
	ds_read_b128 v[148:151], v96 offset:4096
	ds_read_b128 v[152:155], v96 offset:5120
	ds_read_b128 v[156:159], v96 offset:6144
	ds_read_b128 v[160:163], v96 offset:7168
	global_load_lds_dwordx4 v[164:165], off
	v_lshl_add_u64 v[164:165], s[30:31], 0, v[80:81]
	s_mov_b32 m0, s52
	s_nop 0
	global_load_lds_dwordx4 v[164:165], off
	s_waitcnt vmcnt(8)
	s_waitcnt lgkmcnt(0)
	s_barrier
	s_setprio 1
	s_waitcnt lgkmcnt(0)
	v_mfma_f32_16x16x32_bf16 v[62:65], v[100:103], v[132:135], 0
	v_mfma_f32_16x16x32_bf16 v[58:61], v[108:111], v[132:135], 0
	v_mfma_f32_16x16x32_bf16 v[50:53], v[100:103], v[140:143], 0
	v_mfma_f32_16x16x32_bf16 v[42:45], v[108:111], v[140:143], 0
	v_mfma_f32_16x16x32_bf16 v[34:37], v[100:103], v[148:151], 0
	v_mfma_f32_16x16x32_bf16 v[26:29], v[108:111], v[148:151], 0
	v_mfma_f32_16x16x32_bf16 v[18:21], v[100:103], v[156:159], 0
	v_mfma_f32_16x16x32_bf16 v[10:13], v[108:111], v[156:159], 0
	v_mfma_f32_16x16x32_bf16 v[62:65], v[104:107], v[136:139], v[62:65]
	v_mfma_f32_16x16x32_bf16 v[58:61], v[112:115], v[136:139], v[58:61]
	v_mfma_f32_16x16x32_bf16 v[50:53], v[104:107], v[144:147], v[50:53]
	v_mfma_f32_16x16x32_bf16 v[42:45], v[112:115], v[144:147], v[42:45]
	v_mfma_f32_16x16x32_bf16 v[34:37], v[104:107], v[152:155], v[34:37]
	v_mfma_f32_16x16x32_bf16 v[26:29], v[112:115], v[152:155], v[26:29]
	v_mfma_f32_16x16x32_bf16 v[18:21], v[104:107], v[160:163], v[18:21]
	v_mfma_f32_16x16x32_bf16 v[10:13], v[112:115], v[160:163], v[10:13]
	s_setprio 0
	s_setprio 1
	v_mfma_f32_16x16x32_bf16 v[54:57], v[116:119], v[132:135], 0
	v_mfma_f32_16x16x32_bf16 v[46:49], v[124:127], v[132:135], 0
	v_mfma_f32_16x16x32_bf16 v[38:41], v[116:119], v[140:143], 0
	v_mfma_f32_16x16x32_bf16 v[30:33], v[124:127], v[140:143], 0
	v_mfma_f32_16x16x32_bf16 v[22:25], v[116:119], v[148:151], 0
	v_mfma_f32_16x16x32_bf16 v[14:17], v[124:127], v[148:151], 0
	v_mfma_f32_16x16x32_bf16 v[6:9], v[116:119], v[156:159], 0
	v_mfma_f32_16x16x32_bf16 v[2:5], v[124:127], v[156:159], 0
	v_mfma_f32_16x16x32_bf16 v[54:57], v[120:123], v[136:139], v[54:57]
	v_mfma_f32_16x16x32_bf16 v[46:49], v[128:131], v[136:139], v[46:49]
	v_mfma_f32_16x16x32_bf16 v[38:41], v[120:123], v[144:147], v[38:41]
	v_mfma_f32_16x16x32_bf16 v[30:33], v[128:131], v[144:147], v[30:33]
	v_mfma_f32_16x16x32_bf16 v[22:25], v[120:123], v[152:155], v[22:25]
	v_mfma_f32_16x16x32_bf16 v[14:17], v[128:131], v[152:155], v[14:17]
	v_mfma_f32_16x16x32_bf16 v[6:9], v[120:123], v[160:163], v[6:9]
	v_mfma_f32_16x16x32_bf16 v[2:5], v[128:131], v[160:163], v[2:5]
	s_setprio 0
	s_barrier
	s_mov_b32 m0, s53
	v_lshl_add_u64 v[164:165], s[28:29], 0, v[70:71]
	global_load_lds_dwordx4 v[164:165], off
	v_lshl_add_u64 v[166:167], s[28:29], 0, v[66:67]
	s_mov_b32 m0, s58
	v_lshl_add_u64 v[100:101], s[28:29], 0, v[72:73]
	global_load_lds_dwordx4 v[166:167], off
	s_mov_b32 m0, s59
	v_lshl_add_u64 v[168:169], s[26:27], 0, v[74:75]
	global_load_lds_dwordx4 v[100:101], off
	v_lshl_add_u64 v[100:101], s[28:29], 0, v[68:69]
	s_mov_b32 m0, s60
	v_lshl_add_u64 v[172:173], s[26:27], 0, v[76:77]
	global_load_lds_dwordx4 v[100:101], off
	s_mov_b32 m0, s42
	s_nop 0
	global_load_lds_dwordx4 v[168:169], off
	s_mov_b32 m0, s43
	s_nop 0
	global_load_lds_dwordx4 v[172:173], off
	s_waitcnt vmcnt(8)
	s_waitcnt lgkmcnt(0)
	s_barrier
; #define PG8_STAGE(bufoff, gbase, voff) do { _Pragma("unroll") for (int _i = 0; _i < 2; ++_i) \
;         __builtin_amdgcn_global_load_lds((const unsigned*)((const char*)(gbase) + (voff)[_i]), (PG8_LAS unsigned*)(lds + (bufoff) + ldsw + _i * 8192), 16, 0, 0); } while (0)
; #define PG8_WAIT_V(n) asm volatile("s_waitcnt vmcnt(" #n ")" ::: "memory")
; #define PG8_WAIT_L(n) asm volatile("s_waitcnt lgkmcnt(" #n ")" ::: "memory")
; #define PG8_BAR __builtin_amdgcn_s_barrier()
; #define PG8_SCHED __builtin_amdgcn_sched_barrier(0)
; template <class Epi, class Sched, bool ALIGN_EPI = true, bool F8 = false>
; __device__ __forceinline__ void gemm_phase(PG8_LAS unsigned char* lds, const Sched& S, const Epi& E) {
;     ...
;             PG8_WAIT_V(8); PG8_WAIT_L(0); PG8_BAR; PG8_MMA(1, 0, At, B0); PG8_MMA(1, 1, At, B1); PG8_BAR; PG8_SCHED;
;             PG8_LDB(B0, 1, 0); PG8_LDB(B1, 1, 1); PG8_SCHED; PG8_LDA(At, 1, 0); PG8_STAGE(PG8_SA(0, 1), a2, vA2[1]);
;             PG8_WAIT_V(8); PG8_WAIT_L(0); PG8_BAR; PG8_MMA(0, 0, At, B0); PG8_MMA(0, 1, At, B1); PG8_BAR; PG8_SCHED;
;             PG8_LDA(At, 1, 1); PG8_STAGE(PG8_SB(1, 0), b3, voffB[0]); PG8_STAGE(PG8_SB(1, 1), b3, voffB[1]); PG8_STAGE(PG8_SA(1, 0), a3, vA2[0]);
;             PG8_WAIT_V(8); PG8_WAIT_L(0); PG8_BAR; PG8_MMA(1, 0, At, B0); PG8_MMA(1, 1, At, B1); PG8_BAR; PG8_SCHED;
	s_setprio 1
	s_setprio 0
	s_setprio 1
	s_setprio 0
	s_barrier
	ds_read_b128 v[100:103], v97
	ds_read_b128 v[104:107], v97 offset:1024
	ds_read_b128 v[108:111], v97 offset:2048
	ds_read_b128 v[112:115], v97 offset:3072
	ds_read_b128 v[116:119], v98
	ds_read_b128 v[120:123], v98 offset:1024
	ds_read_b128 v[124:127], v98 offset:2048
	ds_read_b128 v[128:131], v98 offset:3072
	s_mov_b32 m0, s44
	v_lshl_add_u64 v[174:175], s[26:27], 0, v[78:79]
	ds_read_b128 v[132:135], v96 offset:32768
	ds_read_b128 v[136:139], v96 offset:33792
	ds_read_b128 v[140:143], v96 offset:34816
	ds_read_b128 v[144:147], v96 offset:35840
	ds_read_b128 v[148:151], v96 offset:36864
	ds_read_b128 v[152:155], v96 offset:37888
	ds_read_b128 v[156:159], v96 offset:38912
	ds_read_b128 v[160:163], v96 offset:39936
	global_load_lds_dwordx4 v[174:175], off
	v_lshl_add_u64 v[174:175], s[26:27], 0, v[80:81]
	s_mov_b32 m0, s45
	s_nop 0
	global_load_lds_dwordx4 v[174:175], off
	s_waitcnt vmcnt(8)
	s_waitcnt lgkmcnt(0)
	s_barrier
	s_setprio 1
	s_waitcnt lgkmcnt(0)
	v_mfma_f32_16x16x32_bf16 v[62:65], v[100:103], v[132:135], v[62:65]
	v_mfma_f32_16x16x32_bf16 v[58:61], v[108:111], v[132:135], v[58:61]
	v_mfma_f32_16x16x32_bf16 v[50:53], v[100:103], v[140:143], v[50:53]
	v_mfma_f32_16x16x32_bf16 v[42:45], v[108:111], v[140:143], v[42:45]
	v_mfma_f32_16x16x32_bf16 v[34:37], v[100:103], v[148:151], v[34:37]
	v_mfma_f32_16x16x32_bf16 v[26:29], v[108:111], v[148:151], v[26:29]
	v_mfma_f32_16x16x32_bf16 v[18:21], v[100:103], v[156:159], v[18:21]
	v_mfma_f32_16x16x32_bf16 v[10:13], v[108:111], v[156:159], v[10:13]
	v_mfma_f32_16x16x32_bf16 v[62:65], v[104:107], v[136:139], v[62:65]
	v_mfma_f32_16x16x32_bf16 v[58:61], v[112:115], v[136:139], v[58:61]
	v_mfma_f32_16x16x32_bf16 v[50:53], v[104:107], v[144:147], v[50:53]
	v_mfma_f32_16x16x32_bf16 v[42:45], v[112:115], v[144:147], v[42:45]
	v_mfma_f32_16x16x32_bf16 v[34:37], v[104:107], v[152:155], v[34:37]
	v_mfma_f32_16x16x32_bf16 v[26:29], v[112:115], v[152:155], v[26:29]
	v_mfma_f32_16x16x32_bf16 v[18:21], v[104:107], v[160:163], v[18:21]
	v_mfma_f32_16x16x32_bf16 v[10:13], v[112:115], v[160:163], v[10:13]
	s_setprio 0
	s_setprio 1
	v_mfma_f32_16x16x32_bf16 v[54:57], v[116:119], v[132:135], v[54:57]
	v_mfma_f32_16x16x32_bf16 v[46:49], v[124:127], v[132:135], v[46:49]
	v_mfma_f32_16x16x32_bf16 v[38:41], v[116:119], v[140:143], v[38:41]
	v_mfma_f32_16x16x32_bf16 v[30:33], v[124:127], v[140:143], v[30:33]
	v_mfma_f32_16x16x32_bf16 v[22:25], v[116:119], v[148:151], v[22:25]
	v_mfma_f32_16x16x32_bf16 v[14:17], v[124:127], v[148:151], v[14:17]
	v_mfma_f32_16x16x32_bf16 v[6:9], v[116:119], v[156:159], v[6:9]
	v_mfma_f32_16x16x32_bf16 v[2:5], v[124:127], v[156:159], v[2:5]
	v_mfma_f32_16x16x32_bf16 v[54:57], v[120:123], v[136:139], v[54:57]
	v_mfma_f32_16x16x32_bf16 v[46:49], v[128:131], v[136:139], v[46:49]
	v_mfma_f32_16x16x32_bf16 v[38:41], v[120:123], v[144:147], v[38:41]
	v_mfma_f32_16x16x32_bf16 v[30:33], v[128:131], v[144:147], v[30:33]
	v_mfma_f32_16x16x32_bf16 v[22:25], v[120:123], v[152:155], v[22:25]
	v_mfma_f32_16x16x32_bf16 v[14:17], v[128:131], v[152:155], v[14:17]
	v_mfma_f32_16x16x32_bf16 v[6:9], v[120:123], v[160:163], v[6:9]
	v_mfma_f32_16x16x32_bf16 v[2:5], v[128:131], v[160:163], v[2:5]
	s_setprio 0
	s_barrier
	s_mov_b32 m0, s61
	v_lshl_add_u64 v[100:101], v[164:165], 0, s[10:11]
	global_load_lds_dwordx4 v[100:101], off
	v_lshl_add_u64 v[100:101], v[166:167], 0, s[10:11]
	s_mov_b32 m0, s62
	s_nop 0
	global_load_lds_dwordx4 v[100:101], off
	v_lshl_add_u64 v[100:101], s[24:25], 0, v[72:73]
	s_mov_b32 m0, s63
	s_nop 0
	global_load_lds_dwordx4 v[100:101], off
	v_lshl_add_u64 v[100:101], s[24:25], 0, v[68:69]
	s_mov_b32 m0, s64
	s_nop 0
	global_load_lds_dwordx4 v[100:101], off
	v_lshl_add_u64 v[100:101], v[168:169], 0, s[10:11]
	s_mov_b32 m0, s47
	s_nop 0
	global_load_lds_dwordx4 v[100:101], off
	v_lshl_add_u64 v[100:101], v[172:173], 0, s[10:11]
	s_mov_b32 m0, s48
	s_nop 0
	global_load_lds_dwordx4 v[100:101], off
	s_waitcnt vmcnt(8)
	s_waitcnt lgkmcnt(0)
	s_barrier
	s_setprio 1
	s_setprio 0
	s_setprio 1
	s_setprio 0
	s_barrier
	s_andn2_b64 vcc, exec, s[22:23]
	s_mov_b64 s[24:25], -1
	s_mov_b64 s[22:23], 0
	s_movk_i32 s19, 0x100
	s_cbranch_vccz .LBB0_692
	s_branch .Lpx_19328

; #define PG8_STAGE(bufoff, gbase, voff) do { _Pragma("unroll") for (int _i = 0; _i < 2; ++_i) \
;         __builtin_amdgcn_global_load_lds((const unsigned*)((const char*)(gbase) + (voff)[_i]), (PG8_LAS unsigned*)(lds + (bufoff) + ldsw + _i * 8192), 16, 0, 0); } while (0)
; #define PG8_WAIT_V(n) asm volatile("s_waitcnt vmcnt(" #n ")" ::: "memory")
; #define PG8_WAIT_L(n) asm volatile("s_waitcnt lgkmcnt(" #n ")" ::: "memory")
; #define PG8_BAR __builtin_amdgcn_s_barrier()
; #define PG8_SCHED __builtin_amdgcn_sched_barrier(0)
; template <class Epi, class Sched, bool ALIGN_EPI = true, bool F8 = false>
; __device__ __forceinline__ void gemm_phase(PG8_LAS unsigned char* lds, const Sched& S, const Epi& E) {
;     ...
;             PG8_LDB(B0, 0, 0); PG8_LDB(B1, 0, 1); PG8_SCHED; PG8_LDA(At, 0, 0); PG8_STAGE(PG8_SA(1, 1), a1, voffA[1]);
;             PG8_WAIT_V(8); PG8_WAIT_L(0); PG8_BAR; PG8_MMA(0, 0, At, B0); PG8_MMA(0, 1, At, B1); PG8_BAR; PG8_SCHED;
;             PG8_LDA(At, 0, 1); PG8_STAGE(PG8_SB(0, 0), b2, voffB[0]); PG8_STAGE(PG8_SB(0, 1), b2, voffB[1]); PG8_STAGE(PG8_SA(0, 0), a2, vA2[0]);
;             PG8_WAIT_V(8); PG8_WAIT_L(0); PG8_BAR; PG8_MMA(1, 0, At, B0); PG8_MMA(1, 1, At, B1); PG8_BAR; PG8_SCHED;
;     ...
;         for (int a = 0; a < 2; ++a)
; #pragma unroll
;             for (int b = 0; b < 2; ++b)
; #pragma unroll
;                 for (int m = 0; m < 4; ++m)
; #pragma unroll
;                     for (int n = 0; n < 2; ++n) acc[a][b][m][n] = (f32x4){0.f, 0.f, 0.f, 0.f};
.LBB0_762:
	s_add_u32 s19, s28, 0x100
	s_addc_u32 s21, s29, 0
	s_add_u32 s26, s26, 0x80
	s_addc_u32 s27, s27, 0
	s_mov_b32 s69, -2
.Lpkb_763:
	ds_read_b128 v[62:65], v208
	ds_read_b128 v[70:73], v208 offset:1024
	ds_read_b128 v[74:77], v208 offset:2048
	ds_read_b128 v[78:81], v208 offset:3072
	ds_read_b128 v[138:141], v209
	ds_read_b128 v[150:153], v209 offset:1024
	ds_read_b128 v[154:157], v209 offset:2048
	ds_read_b128 v[158:161], v209 offset:3072
	s_add_u32 s28, s26, 0x80
	s_addc_u32 s29, s27, 0
	s_cmp_eq_u32 s69, 4
	s_cselect_b32 s31, s23, s29
	s_cselect_b32 s30, s22, s28
	s_cselect_b32 s29, s25, s21
	s_cselect_b32 s28, s24, s19
	v_lshl_add_u64 v[236:237], s[26:27], 0, v[196:197]
	s_add_i32 m0, s44, 0xc000
	ds_read_b128 v[162:165], v210
	ds_read_b128 v[166:169], v210 offset:1024
	ds_read_b128 v[202:205], v210 offset:2048
	ds_read_b128 v[216:219], v210 offset:3072
	ds_read_b128 v[220:223], v210 offset:4096
	ds_read_b128 v[224:227], v210 offset:5120
	ds_read_b128 v[228:231], v210 offset:6144
	ds_read_b128 v[232:235], v210 offset:7168
	global_load_lds_dwordx4 v[236:237], off
	v_lshl_add_u64 v[236:237], s[26:27], 0, v[194:195]
	s_add_i32 m0, s44, 0xe000
	s_nop 0
	global_load_lds_dwordx4 v[236:237], off
	s_waitcnt vmcnt(8)
	s_waitcnt lgkmcnt(0)
	s_barrier
	s_setprio 1
	s_waitcnt lgkmcnt(0)
	v_mfma_f32_16x16x32_bf16 v[146:149], v[62:65], v[162:165], 0
	v_mfma_f32_16x16x32_bf16 v[142:145], v[74:77], v[162:165], 0
	v_mfma_f32_16x16x32_bf16 v[126:129], v[62:65], v[202:205], 0
	v_mfma_f32_16x16x32_bf16 v[122:125], v[74:77], v[202:205], 0
	v_mfma_f32_16x16x32_bf16 v[110:113], v[62:65], v[220:223], 0
	v_mfma_f32_16x16x32_bf16 v[106:109], v[74:77], v[220:223], 0
	v_mfma_f32_16x16x32_bf16 v[94:97], v[62:65], v[228:231], 0
	v_mfma_f32_16x16x32_bf16 v[90:93], v[74:77], v[228:231], 0
	v_mfma_f32_16x16x32_bf16 v[146:149], v[70:73], v[166:169], v[146:149]
	v_mfma_f32_16x16x32_bf16 v[142:145], v[78:81], v[166:169], v[142:145]
	v_mfma_f32_16x16x32_bf16 v[126:129], v[70:73], v[216:219], v[126:129]
	v_mfma_f32_16x16x32_bf16 v[122:125], v[78:81], v[216:219], v[122:125]
	v_mfma_f32_16x16x32_bf16 v[110:113], v[70:73], v[224:227], v[110:113]
	v_mfma_f32_16x16x32_bf16 v[106:109], v[78:81], v[224:227], v[106:109]
	v_mfma_f32_16x16x32_bf16 v[94:97], v[70:73], v[232:235], v[94:97]
	v_mfma_f32_16x16x32_bf16 v[90:93], v[78:81], v[232:235], v[90:93]
	s_setprio 0
	s_setprio 1
	v_mfma_f32_16x16x32_bf16 v[134:137], v[138:141], v[162:165], 0
	v_mfma_f32_16x16x32_bf16 v[130:133], v[154:157], v[162:165], 0
	v_mfma_f32_16x16x32_bf16 v[118:121], v[138:141], v[202:205], 0
	v_mfma_f32_16x16x32_bf16 v[114:117], v[154:157], v[202:205], 0
	v_mfma_f32_16x16x32_bf16 v[102:105], v[138:141], v[220:223], 0
	v_mfma_f32_16x16x32_bf16 v[98:101], v[154:157], v[220:223], 0
	v_mfma_f32_16x16x32_bf16 v[86:89], v[138:141], v[228:231], 0
	v_mfma_f32_16x16x32_bf16 v[82:85], v[154:157], v[228:231], 0
	v_mfma_f32_16x16x32_bf16 v[134:137], v[150:153], v[166:169], v[134:137]
	v_mfma_f32_16x16x32_bf16 v[130:133], v[158:161], v[166:169], v[130:133]
	v_mfma_f32_16x16x32_bf16 v[118:121], v[150:153], v[216:219], v[118:121]
	v_mfma_f32_16x16x32_bf16 v[114:117], v[158:161], v[216:219], v[114:117]
	v_mfma_f32_16x16x32_bf16 v[102:105], v[150:153], v[224:227], v[102:105]
	v_mfma_f32_16x16x32_bf16 v[98:101], v[158:161], v[224:227], v[98:101]
	v_mfma_f32_16x16x32_bf16 v[86:89], v[150:153], v[232:235], v[86:89]
	v_mfma_f32_16x16x32_bf16 v[82:85], v[158:161], v[232:235], v[82:85]
	s_setprio 0
	s_barrier
	s_add_i32 s70, s60, s43
	v_lshl_add_u64 v[236:237], s[28:29], 0, v[172:173]
	s_mov_b32 m0, s70
	ds_read_b128 v[162:165], v210 offset:16384
	ds_read_b128 v[166:169], v210 offset:17408
	ds_read_b128 v[202:205], v210 offset:18432
	ds_read_b128 v[216:219], v210 offset:19456
	ds_read_b128 v[220:223], v210 offset:20480
	ds_read_b128 v[224:227], v210 offset:21504
	ds_read_b128 v[228:231], v210 offset:22528
	ds_read_b128 v[232:235], v210 offset:23552
	global_load_lds_dwordx4 v[236:237], off
	v_lshl_add_u64 v[238:239], s[28:29], 0, v[174:175]
	s_add_i32 m0, s70, 0x2000
	s_add_i32 s70, s61, s43
	global_load_lds_dwordx4 v[238:239], off
	v_lshl_add_u64 v[240:241], s[28:29], 0, v[176:177]
	s_mov_b32 m0, s70
	v_lshl_add_u64 v[242:243], s[30:31], 0, v[182:183]
	global_load_lds_dwordx4 v[240:241], off
	v_lshl_add_u64 v[240:241], s[28:29], 0, v[178:179]
	s_add_i32 m0, s70, 0x2000
	s_nop 0
	global_load_lds_dwordx4 v[240:241], off
	v_lshl_add_u64 v[240:241], s[30:31], 0, v[180:181]
	s_mov_b32 m0, s44
	s_nop 0
	global_load_lds_dwordx4 v[240:241], off
	s_mov_b32 m0, s45
	s_nop 0
	global_load_lds_dwordx4 v[242:243], off
	s_waitcnt vmcnt(8)
	s_waitcnt lgkmcnt(0)
	s_barrier
; #define PG8_STAGE(bufoff, gbase, voff) do { _Pragma("unroll") for (int _i = 0; _i < 2; ++_i) \
;         __builtin_amdgcn_global_load_lds((const unsigned*)((const char*)(gbase) + (voff)[_i]), (PG8_LAS unsigned*)(lds + (bufoff) + ldsw + _i * 8192), 16, 0, 0); } while (0)
; #define PG8_WAIT_V(n) asm volatile("s_waitcnt vmcnt(" #n ")" ::: "memory")
; #define PG8_WAIT_L(n) asm volatile("s_waitcnt lgkmcnt(" #n ")" ::: "memory")
; #define PG8_BAR __builtin_amdgcn_s_barrier()
; #define PG8_SCHED __builtin_amdgcn_sched_barrier(0)
; template <class Epi, class Sched, bool ALIGN_EPI = true, bool F8 = false>
; __device__ __forceinline__ void gemm_phase(PG8_LAS unsigned char* lds, const Sched& S, const Epi& E) {
;     ...
;             PG8_WAIT_V(8); PG8_WAIT_L(0); PG8_BAR; PG8_MMA(1, 0, At, B0); PG8_MMA(1, 1, At, B1); PG8_BAR; PG8_SCHED;
;             PG8_LDB(B0, 1, 0); PG8_LDB(B1, 1, 1); PG8_SCHED; PG8_LDA(At, 1, 0); PG8_STAGE(PG8_SA(0, 1), a2, vA2[1]);
;             PG8_WAIT_V(8); PG8_WAIT_L(0); PG8_BAR; PG8_MMA(0, 0, At, B0); PG8_MMA(0, 1, At, B1); PG8_BAR; PG8_SCHED;
	s_setprio 1
	s_waitcnt lgkmcnt(0)
	v_mfma_f32_16x16x32_bf16 v[66:69], v[62:65], v[162:165], 0
	v_mfma_f32_16x16x32_bf16 v[58:61], v[74:77], v[162:165], 0
	v_mfma_f32_16x16x32_bf16 v[46:49], v[62:65], v[202:205], 0
	v_mfma_f32_16x16x32_bf16 v[42:45], v[74:77], v[202:205], 0
	v_mfma_f32_16x16x32_bf16 v[30:33], v[62:65], v[220:223], 0
	v_mfma_f32_16x16x32_bf16 v[26:29], v[74:77], v[220:223], 0
	v_mfma_f32_16x16x32_bf16 v[14:17], v[62:65], v[228:231], 0
	v_mfma_f32_16x16x32_bf16 v[10:13], v[74:77], v[228:231], 0
	v_mfma_f32_16x16x32_bf16 v[66:69], v[70:73], v[166:169], v[66:69]
	v_mfma_f32_16x16x32_bf16 v[58:61], v[78:81], v[166:169], v[58:61]
	v_mfma_f32_16x16x32_bf16 v[46:49], v[70:73], v[216:219], v[46:49]
	v_mfma_f32_16x16x32_bf16 v[42:45], v[78:81], v[216:219], v[42:45]
	v_mfma_f32_16x16x32_bf16 v[30:33], v[70:73], v[224:227], v[30:33]
	v_mfma_f32_16x16x32_bf16 v[26:29], v[78:81], v[224:227], v[26:29]
	v_mfma_f32_16x16x32_bf16 v[14:17], v[70:73], v[232:235], v[14:17]
	v_mfma_f32_16x16x32_bf16 v[10:13], v[78:81], v[232:235], v[10:13]
	s_setprio 0
	s_setprio 1
	v_mfma_f32_16x16x32_bf16 v[54:57], v[138:141], v[162:165], 0
	v_mfma_f32_16x16x32_bf16 v[50:53], v[154:157], v[162:165], 0
	v_mfma_f32_16x16x32_bf16 v[38:41], v[138:141], v[202:205], 0
	v_mfma_f32_16x16x32_bf16 v[34:37], v[154:157], v[202:205], 0
	v_mfma_f32_16x16x32_bf16 v[22:25], v[138:141], v[220:223], 0
	v_mfma_f32_16x16x32_bf16 v[18:21], v[154:157], v[220:223], 0
	v_mfma_f32_16x16x32_bf16 v[6:9], v[138:141], v[228:231], 0
	v_mfma_f32_16x16x32_bf16 v[2:5], v[154:157], v[228:231], 0
	v_mfma_f32_16x16x32_bf16 v[54:57], v[150:153], v[166:169], v[54:57]
	v_mfma_f32_16x16x32_bf16 v[50:53], v[158:161], v[166:169], v[50:53]
	v_mfma_f32_16x16x32_bf16 v[38:41], v[150:153], v[216:219], v[38:41]
	v_mfma_f32_16x16x32_bf16 v[34:37], v[158:161], v[216:219], v[34:37]
	v_mfma_f32_16x16x32_bf16 v[22:25], v[150:153], v[224:227], v[22:25]
	v_mfma_f32_16x16x32_bf16 v[18:21], v[158:161], v[224:227], v[18:21]
	v_mfma_f32_16x16x32_bf16 v[6:9], v[150:153], v[232:235], v[6:9]
	v_mfma_f32_16x16x32_bf16 v[2:5], v[158:161], v[232:235], v[2:5]
	s_setprio 0
	s_barrier
	s_add_i32 s70, 0, 0x18000
	s_add_i32 s71, 0, 0x1c000
	v_add_u32_e32 v78, s70, v207
	v_add_u32_e32 v158, s71, v207
	ds_read_b128 v[62:65], v78
	ds_read_b128 v[70:73], v78 offset:1024
	ds_read_b128 v[74:77], v78 offset:2048
	ds_read_b128 v[78:81], v78 offset:3072
	ds_read_b128 v[138:141], v158
	ds_read_b128 v[150:153], v158 offset:1024
	ds_read_b128 v[154:157], v158 offset:2048
	ds_read_b128 v[158:161], v158 offset:3072
	s_mov_b32 m0, s46
	v_lshl_add_u64 v[244:245], s[30:31], 0, v[184:185]
	ds_read_b128 v[162:165], v210 offset:32768
	ds_read_b128 v[166:169], v210 offset:33792
	ds_read_b128 v[202:205], v210 offset:34816
	ds_read_b128 v[216:219], v210 offset:35840
	ds_read_b128 v[220:223], v210 offset:36864
	ds_read_b128 v[224:227], v210 offset:37888
	ds_read_b128 v[228:231], v210 offset:38912
	ds_read_b128 v[232:235], v210 offset:39936
	global_load_lds_dwordx4 v[244:245], off
	v_lshl_add_u64 v[244:245], s[30:31], 0, v[186:187]
	s_mov_b32 m0, s47
	s_nop 0
	global_load_lds_dwordx4 v[244:245], off
	s_waitcnt vmcnt(8)
	s_waitcnt lgkmcnt(0)
	s_barrier
	s_setprio 1
	s_waitcnt lgkmcnt(0)
	v_mfma_f32_16x16x32_bf16 v[146:149], v[62:65], v[162:165], v[146:149]
	v_mfma_f32_16x16x32_bf16 v[142:145], v[74:77], v[162:165], v[142:145]
	v_mfma_f32_16x16x32_bf16 v[126:129], v[62:65], v[202:205], v[126:129]
	v_mfma_f32_16x16x32_bf16 v[122:125], v[74:77], v[202:205], v[122:125]
	v_mfma_f32_16x16x32_bf16 v[110:113], v[62:65], v[220:223], v[110:113]
	v_mfma_f32_16x16x32_bf16 v[106:109], v[74:77], v[220:223], v[106:109]
	v_mfma_f32_16x16x32_bf16 v[94:97], v[62:65], v[228:231], v[94:97]
	v_mfma_f32_16x16x32_bf16 v[90:93], v[74:77], v[228:231], v[90:93]
	v_mfma_f32_16x16x32_bf16 v[146:149], v[70:73], v[166:169], v[146:149]
	v_mfma_f32_16x16x32_bf16 v[142:145], v[78:81], v[166:169], v[142:145]
	v_mfma_f32_16x16x32_bf16 v[126:129], v[70:73], v[216:219], v[126:129]
	v_mfma_f32_16x16x32_bf16 v[122:125], v[78:81], v[216:219], v[122:125]
	v_mfma_f32_16x16x32_bf16 v[110:113], v[70:73], v[224:227], v[110:113]
	v_mfma_f32_16x16x32_bf16 v[106:109], v[78:81], v[224:227], v[106:109]
	v_mfma_f32_16x16x32_bf16 v[94:97], v[70:73], v[232:235], v[94:97]
	v_mfma_f32_16x16x32_bf16 v[90:93], v[78:81], v[232:235], v[90:93]
	s_setprio 0
	s_setprio 1
	v_mfma_f32_16x16x32_bf16 v[134:137], v[138:141], v[162:165], v[134:137]
	v_mfma_f32_16x16x32_bf16 v[130:133], v[154:157], v[162:165], v[130:133]
	v_mfma_f32_16x16x32_bf16 v[118:121], v[138:141], v[202:205], v[118:121]
	v_mfma_f32_16x16x32_bf16 v[114:117], v[154:157], v[202:205], v[114:117]
	v_mfma_f32_16x16x32_bf16 v[102:105], v[138:141], v[220:223], v[102:105]
	v_mfma_f32_16x16x32_bf16 v[98:101], v[154:157], v[220:223], v[98:101]
	v_mfma_f32_16x16x32_bf16 v[86:89], v[138:141], v[228:231], v[86:89]
	v_mfma_f32_16x16x32_bf16 v[82:85], v[154:157], v[228:231], v[82:85]
	v_mfma_f32_16x16x32_bf16 v[134:137], v[150:153], v[166:169], v[134:137]
	v_mfma_f32_16x16x32_bf16 v[130:133], v[158:161], v[166:169], v[130:133]
	v_mfma_f32_16x16x32_bf16 v[118:121], v[150:153], v[216:219], v[118:121]
	v_mfma_f32_16x16x32_bf16 v[114:117], v[158:161], v[216:219], v[114:117]
	v_mfma_f32_16x16x32_bf16 v[102:105], v[150:153], v[224:227], v[102:105]
	v_mfma_f32_16x16x32_bf16 v[98:101], v[158:161], v[224:227], v[98:101]
	v_mfma_f32_16x16x32_bf16 v[86:89], v[150:153], v[232:235], v[86:89]
	v_mfma_f32_16x16x32_bf16 v[82:85], v[158:161], v[232:235], v[82:85]
	s_setprio 0
	s_barrier
; #define PG8_STAGE(bufoff, gbase, voff) do { _Pragma("unroll") for (int _i = 0; _i < 2; ++_i) \
;         __builtin_amdgcn_global_load_lds((const unsigned*)((const char*)(gbase) + (voff)[_i]), (PG8_LAS unsigned*)(lds + (bufoff) + ldsw + _i * 8192), 16, 0, 0); } while (0)
; #define PG8_WAIT_V(n) asm volatile("s_waitcnt vmcnt(" #n ")" ::: "memory")
; #define PG8_WAIT_L(n) asm volatile("s_waitcnt lgkmcnt(" #n ")" ::: "memory")
; #define PG8_BAR __builtin_amdgcn_s_barrier()
; #define PG8_SCHED __builtin_amdgcn_sched_barrier(0)
; template <class Epi, class Sched, bool ALIGN_EPI = true, bool F8 = false>
; __device__ __forceinline__ void gemm_phase(PG8_LAS unsigned char* lds, const Sched& S, const Epi& E) {
;     ...
;         for (int t = 0; t < nt; t += 2) {
;     ...
;             PG8_LDA(At, 1, 1); PG8_STAGE(PG8_SB(1, 0), b3, voffB[0]); PG8_STAGE(PG8_SB(1, 1), b3, voffB[1]); PG8_STAGE(PG8_SA(1, 0), a3, vA2[0]);
;             PG8_WAIT_V(8); PG8_WAIT_L(0); PG8_BAR; PG8_MMA(1, 0, At, B0); PG8_MMA(1, 1, At, B1); PG8_BAR; PG8_SCHED;
	s_add_u32 s28, s28, 0x80
	s_addc_u32 s29, s29, 0
	s_add_i32 s30, s70, s43
	v_lshl_add_u64 v[236:237], v[236:237], 0, s[14:15]
	s_mov_b32 m0, s30
	ds_read_b128 v[162:165], v210 offset:49152
	ds_read_b128 v[166:169], v210 offset:50176
	ds_read_b128 v[202:205], v210 offset:51200
	ds_read_b128 v[216:219], v210 offset:52224
	ds_read_b128 v[220:223], v210 offset:53248
	ds_read_b128 v[224:227], v210 offset:54272
	ds_read_b128 v[228:231], v210 offset:55296
	ds_read_b128 v[232:235], v210 offset:56320
	global_load_lds_dwordx4 v[236:237], off
	v_lshl_add_u64 v[236:237], v[238:239], 0, s[14:15]
	s_add_i32 m0, s30, 0x2000
	s_add_i32 s30, s71, s43
	global_load_lds_dwordx4 v[236:237], off
	v_lshl_add_u64 v[236:237], s[28:29], 0, v[176:177]
	s_mov_b32 m0, s30
	s_nop 0
	global_load_lds_dwordx4 v[236:237], off
	v_lshl_add_u64 v[236:237], s[28:29], 0, v[178:179]
	s_add_i32 m0, s30, 0x2000
	s_nop 0
	global_load_lds_dwordx4 v[236:237], off
	v_lshl_add_u64 v[236:237], v[240:241], 0, s[14:15]
	s_mov_b32 m0, s50
	s_nop 0
	global_load_lds_dwordx4 v[236:237], off
	v_lshl_add_u64 v[236:237], v[242:243], 0, s[14:15]
	s_mov_b32 m0, s51
	s_nop 0
	global_load_lds_dwordx4 v[236:237], off
	s_waitcnt vmcnt(8)
	s_waitcnt lgkmcnt(0)
	s_barrier
	s_setprio 1
	s_waitcnt lgkmcnt(0)
	v_mfma_f32_16x16x32_bf16 v[66:69], v[62:65], v[162:165], v[66:69]
	v_mfma_f32_16x16x32_bf16 v[58:61], v[74:77], v[162:165], v[58:61]
	v_mfma_f32_16x16x32_bf16 v[46:49], v[62:65], v[202:205], v[46:49]
	v_mfma_f32_16x16x32_bf16 v[42:45], v[74:77], v[202:205], v[42:45]
	v_mfma_f32_16x16x32_bf16 v[30:33], v[62:65], v[220:223], v[30:33]
	v_mfma_f32_16x16x32_bf16 v[26:29], v[74:77], v[220:223], v[26:29]
	v_mfma_f32_16x16x32_bf16 v[14:17], v[62:65], v[228:231], v[14:17]
	v_mfma_f32_16x16x32_bf16 v[10:13], v[74:77], v[228:231], v[10:13]
	v_mfma_f32_16x16x32_bf16 v[66:69], v[70:73], v[166:169], v[66:69]
	v_mfma_f32_16x16x32_bf16 v[58:61], v[78:81], v[166:169], v[58:61]
	v_mfma_f32_16x16x32_bf16 v[46:49], v[70:73], v[216:219], v[46:49]
	v_mfma_f32_16x16x32_bf16 v[42:45], v[78:81], v[216:219], v[42:45]
	v_mfma_f32_16x16x32_bf16 v[30:33], v[70:73], v[224:227], v[30:33]
	v_mfma_f32_16x16x32_bf16 v[26:29], v[78:81], v[224:227], v[26:29]
	v_mfma_f32_16x16x32_bf16 v[14:17], v[70:73], v[232:235], v[14:17]
	v_mfma_f32_16x16x32_bf16 v[10:13], v[78:81], v[232:235], v[10:13]
	s_setprio 0
	s_setprio 1
	v_mfma_f32_16x16x32_bf16 v[54:57], v[138:141], v[162:165], v[54:57]
	v_mfma_f32_16x16x32_bf16 v[50:53], v[154:157], v[162:165], v[50:53]
	v_mfma_f32_16x16x32_bf16 v[38:41], v[138:141], v[202:205], v[38:41]
	v_mfma_f32_16x16x32_bf16 v[34:37], v[154:157], v[202:205], v[34:37]
	v_mfma_f32_16x16x32_bf16 v[22:25], v[138:141], v[220:223], v[22:25]
	v_mfma_f32_16x16x32_bf16 v[18:21], v[154:157], v[220:223], v[18:21]
	v_mfma_f32_16x16x32_bf16 v[6:9], v[138:141], v[228:231], v[6:9]
	v_mfma_f32_16x16x32_bf16 v[2:5], v[154:157], v[228:231], v[2:5]
	v_mfma_f32_16x16x32_bf16 v[54:57], v[150:153], v[166:169], v[54:57]
	v_mfma_f32_16x16x32_bf16 v[50:53], v[158:161], v[166:169], v[50:53]
	v_mfma_f32_16x16x32_bf16 v[38:41], v[150:153], v[216:219], v[38:41]
	v_mfma_f32_16x16x32_bf16 v[34:37], v[158:161], v[216:219], v[34:37]
	v_mfma_f32_16x16x32_bf16 v[22:25], v[150:153], v[224:227], v[22:25]
	v_mfma_f32_16x16x32_bf16 v[18:21], v[158:161], v[224:227], v[18:21]
	v_mfma_f32_16x16x32_bf16 v[6:9], v[150:153], v[232:235], v[6:9]
	v_mfma_f32_16x16x32_bf16 v[2:5], v[158:161], v[232:235], v[2:5]
	s_setprio 0
	s_barrier
	s_add_i32 s69, s69, 2
	s_add_u32 s19, s19, 0x100
	s_addc_u32 s21, s21, 0
	s_add_u32 s26, s26, 0x100
	s_addc_u32 s27, s27, 0
	s_cmp_gt_u32 s69, 5
	s_cbranch_scc0 .LBB0_763
	s_branch .Lpx_20766
